# fp8 GEMM epilogues: 48 of the 64 dead wait states at the epilogue entry dropped (plus attention loop-edge edit)
# speedup vs baseline: 1.0042x; 1.0015x over previous
; #define LAS __attribute__((address_space(3)))
;     ...
;         if constexpr (FP8) { asm volatile("s_nop 15\n\ts_nop 15\n\ts_nop 15\n\ts_nop 15" ::: "memory"); }
;     __device__ __forceinline__ void operator()(const f32x4 (&acc)[2][2][4][2], const Unit& u, int wr, int wc, int fr, int fq) const {
;         const int pn = u.pn, grp = pn >= 3 ? 1 : 0, pl = pn - 3 * grp;
;         const bool isq = pl < 2, isv = (pl == 2) && (wc >= 2), lat = u.pm < (NLAT / 256);
;         const float* gam = gam4 + (grp * 2 + (isq ? 0 : 1)) * 64;
;         f32x4 gv[2][2];
; #pragma unroll
;         for (int bj = 0; bj < 2; ++bj)
; #pragma unroll
;             for (int n = 0; n < 2; ++n) gv[bj][n] = *(const f32x4*)(gam + 32 * bj + 16 * n + 4 * fq);
;         const float qs = isq ? C2 : 1.f;
;         constexpr float ds = 1.0f / (SC_W * SC_H2);
;         constexpr float EPSA = EPS / (ds * ds);
; #pragma unroll
;         for (int ai = 0; ai < 2; ++ai)
; #pragma unroll
;             for (int m = 0; m < 4; ++m) {
;                 const int r = u.pm * BM + ai * HALF + wr * 64 + m * 16 + fr;
;                 f32x4 v[2][2];
;                 if (ai == 0 && m == 0) __builtin_amdgcn_s_waitcnt(0x0F70);
;                 if (!isv) {
;                     const f32x4 s4 = (acc[ai][0][m][0] * acc[ai][0][m][0] + acc[ai][0][m][1] * acc[ai][0][m][1]) + (acc[ai][1][m][0] * acc[ai][1][m][0] + acc[ai][1][m][1] * acc[ai][1][m][1]);
;                     float ss = (s4[0] + s4[1]) + (s4[2] + s4[3]);
;                     ss += __shfl_xor(ss, 16); ss += __shfl_xor(ss, 32);
;                     const float rs = __builtin_amdgcn_rsqf(ss * (1.0f / 64.0f) + EPSA) * qs;
; #pragma unroll
;                     for (int bj = 0; bj < 2; ++bj)
; #pragma unroll
;                         for (int n = 0; n < 2; ++n) v[bj][n] = acc[ai][bj][m][n] * (gv[bj][n] * rs);
;                     if (lat) {
; #pragma unroll
;                         for (int bj = 0; bj < 2; ++bj) { const int pos = bj ? (m * 16 + fr) : ((u.pm & 7) * 4 + ai * 2 + wr);
;                             const f32x4 cx = *(const LAS f32x4*)(ropeL + pos * 32 + 4 * fq), cy = *(const LAS f32x4*)(ropeL + pos * 32 + 16 + 4 * fq), a = v[bj][0], b = v[bj][1];
;                             v[bj][0] = a * cx - b * cy; v[bj][1] = a * cy + b * cx; }
.LBB0_673:
	s_cmp_gt_i32 s6, 2
	s_cselect_b64 s[28:29], -1, 0
	s_and_b64 s[8:9], s[28:29], exec
	s_cselect_b32 s3, -3, 0
	s_cselect_b32 s12, 2, 0
	s_add_i32 s3, s3, s6
	s_cmp_lt_i32 s3, 2
	s_cselect_b64 s[8:9], -1, 0
	s_cmp_gt_i32 s3, 1
	s_cselect_b64 s[30:31], -1, 0
	v_cndmask_b32_e64 v2, 0, 1, s[30:31]
	v_or_b32_e32 v2, s12, v2
	v_lshlrev_b32_e32 v190, 8, v2
	s_nop 15
	v_lshl_add_u64 v[2:3], v[168:169], 0, v[190:191]
	global_load_dwordx4 v[14:17], v[2:3], off
	global_load_dwordx4 v[10:13], v[2:3], off offset:64
	global_load_dwordx4 v[6:9], v[2:3], off offset:128
	s_nop 0
	global_load_dwordx4 v[2:5], v[2:3], off offset:192
	s_cmp_lg_u32 s3, 2
	s_cselect_b64 s[6:7], -1, 0
	s_or_b64 s[6:7], s[6:7], s[22:23]
	s_cmpk_lt_i32 s2, 0x80
	s_cselect_b64 s[38:39], -1, 0
	v_cndmask_b32_e64 v173, v213, 1.0, s[30:31]
	s_lshl_b32 s30, s2, 2
	s_and_b32 s30, s30, 28
	v_cndmask_b32_e64 v18, 0, 1, s[38:39]
	s_mov_b64 s[18:19], -1
	s_add_i32 s30, s30, s33
	s_and_b64 vcc, exec, s[6:7]
	v_cmp_ne_u32_e64 s[38:39], 1, v18
	s_waitcnt vmcnt(0)
	s_cbranch_vccz .LBB0_677
	v_pk_mul_f32 v[18:19], v[152:153], v[152:153]
	v_pk_mul_f32 v[20:21], v[150:151], v[150:151]
	v_pk_mul_f32 v[22:23], v[160:161], v[160:161]
	v_pk_mul_f32 v[24:25], v[158:159], v[158:159]
	v_pk_fma_f32 v[18:19], v[148:149], v[148:149], v[18:19]
	v_pk_fma_f32 v[20:21], v[146:147], v[146:147], v[20:21]
	v_pk_fma_f32 v[22:23], v[156:157], v[156:157], v[22:23]
	v_pk_fma_f32 v[24:25], v[154:155], v[154:155], v[24:25]
	v_pk_add_f32 v[18:19], v[18:19], v[22:23]
	v_pk_add_f32 v[20:21], v[20:21], v[24:25]
	s_nop 0
	v_pk_mov_b32 v[22:23], v[20:21], v[18:19] op_sel:[1,0]
	v_mov_b32_e32 v21, v19
	v_pk_add_f32 v[18:19], v[22:23], v[20:21]
	v_and_b32_e32 v20, 64, v211
	v_add_f32_e32 v18, v18, v19
	v_xor_b32_e32 v19, 16, v211
	v_add_u32_e32 v20, 64, v20
	v_cmp_lt_i32_e32 vcc, v19, v20
	s_nop 1
	v_cndmask_b32_e32 v19, v211, v19, vcc
	v_lshlrev_b32_e32 v19, 2, v19
	ds_bpermute_b32 v19, v19, v18
	s_waitcnt lgkmcnt(0)
	v_add_f32_e32 v18, v18, v19
	v_xor_b32_e32 v19, 32, v211
	v_cmp_lt_i32_e32 vcc, v19, v20
	s_nop 1
	v_cndmask_b32_e32 v19, v211, v19, vcc
	v_lshlrev_b32_e32 v19, 2, v19
	ds_bpermute_b32 v19, v19, v18
	s_and_b64 vcc, exec, s[38:39]
	s_waitcnt lgkmcnt(0)
	v_add_f32_e32 v18, v18, v19
	v_fmamk_f32 v18, v18, 0x3c800000, v210
	v_rsq_f32_e32 v18, v18
	s_nop 0
	v_mul_f32_e32 v26, v173, v18
	v_pk_mul_f32 v[18:19], v[14:15], v[26:27] op_sel_hi:[1,0]
	v_pk_mul_f32 v[20:21], v[16:17], v[26:27] op_sel_hi:[1,0]
	v_pk_mul_f32 v[30:31], v[146:147], v[18:19]
	v_pk_mul_f32 v[32:33], v[148:149], v[20:21]
	v_pk_mul_f32 v[18:19], v[10:11], v[26:27] op_sel_hi:[1,0]
	v_pk_mul_f32 v[20:21], v[12:13], v[26:27] op_sel_hi:[1,0]
	v_pk_mul_f32 v[22:23], v[6:7], v[26:27] op_sel_hi:[1,0]
	v_pk_mul_f32 v[24:25], v[8:9], v[26:27] op_sel_hi:[1,0]
	v_pk_mul_f32 v[174:175], v[2:3], v[26:27] op_sel_hi:[1,0]
	v_pk_mul_f32 v[26:27], v[4:5], v[26:27] op_sel_hi:[1,0]
	v_pk_mul_f32 v[20:21], v[152:153], v[20:21]
	v_pk_mul_f32 v[18:19], v[150:151], v[18:19]
	v_pk_mul_f32 v[24:25], v[156:157], v[24:25]
	v_pk_mul_f32 v[22:23], v[154:155], v[22:23]
	v_pk_mul_f32 v[28:29], v[160:161], v[26:27]
	v_pk_mul_f32 v[26:27], v[158:159], v[174:175]
	s_cbranch_vccnz .LBB0_676
	v_lshl_add_u32 v178, s30, 7, v170
	ds_read_b128 v[174:177], v178
	ds_read_b128 v[178:181], v178 offset:64
	s_waitcnt lgkmcnt(0)
	v_pk_mul_f32 v[182:183], v[20:21], v[180:181]
	v_pk_mul_f32 v[186:187], v[18:19], v[178:179]
	v_pk_fma_f32 v[184:185], v[32:33], v[176:177], v[182:183] neg_lo:[0,0,1] neg_hi:[0,0,1]
	v_pk_fma_f32 v[182:183], v[30:31], v[174:175], v[186:187] neg_lo:[0,0,1] neg_hi:[0,0,1]
	v_pk_mul_f32 v[32:33], v[32:33], v[180:181]
	v_pk_mul_f32 v[30:31], v[30:31], v[178:179]
	v_pk_fma_f32 v[20:21], v[20:21], v[176:177], v[32:33]
	v_pk_fma_f32 v[18:19], v[18:19], v[174:175], v[30:31]
	ds_read_b128 v[30:33], v171
	ds_read_b128 v[174:177], v171 offset:64
	s_waitcnt lgkmcnt(0)
	v_pk_mul_f32 v[178:179], v[28:29], v[176:177]
	v_pk_mul_f32 v[186:187], v[26:27], v[174:175]
	v_pk_fma_f32 v[180:181], v[24:25], v[32:33], v[178:179] neg_lo:[0,0,1] neg_hi:[0,0,1]
	v_pk_fma_f32 v[178:179], v[22:23], v[30:31], v[186:187] neg_lo:[0,0,1] neg_hi:[0,0,1]
	v_pk_mul_f32 v[24:25], v[24:25], v[176:177]
	v_pk_mul_f32 v[22:23], v[22:23], v[174:175]
	v_pk_fma_f32 v[28:29], v[28:29], v[32:33], v[24:25]
	v_pk_fma_f32 v[26:27], v[26:27], v[30:31], v[22:23]
	v_mov_b64_e32 v[30:31], v[182:183]
	v_mov_b64_e32 v[22:23], v[178:179]
	v_mov_b64_e32 v[32:33], v[184:185]
	v_mov_b64_e32 v[24:25], v[180:181]

; #define GAS __attribute__((address_space(1)))
; __device__ __forceinline__ unsigned cvt_pk_bf16(float lo, float hi) { unsigned r; asm volatile("v_cvt_pk_bf16_f32 %0, %1, %2" : "=v"(r) : "v"(lo), "v"(hi)); return r; }
; #define RESID_LD(j) do { _Pragma("unroll") for (int bj = 0; bj < 2; ++bj) xv[j][bj] = *(const GAS u32x4*)(X + (size_t)(row0 + ((j) >> 2) * HALF + ((j) & 3) * 16) * D + col0 + bj * HALF); } while (0)
;     ...
;         if constexpr (FP8) { asm volatile("s_nop 15\n\ts_nop 15\n\ts_nop 15\n\ts_nop 15" ::: "memory"); }
;     __device__ __forceinline__ void operator()(const f32x4 (&acc)[2][2][4][2], const Unit& u, int wr, int wc, int fr, int fq) const {
;         const int b = u.pm < (NLAT / 256) ? (u.pm >> 3) : 16;
;         const float* g = modL + b * 6144 + goff;
;         const int row0 = u.pm * BM + wr * 64 + fr, col0 = u.pn * BM + wc * 32 + 8 * fq;
;         f32x4 gv[2][2];
; #pragma unroll
;         for (int bj = 0; bj < 2; ++bj)
; #pragma unroll
;             for (int n = 0; n < 2; ++n) gv[bj][n] = *(const f32x4*)(g + col0 + bj * HALF + 4 * n) * ds;
;         constexpr int XPF = RESID_XPF;
;         u32x4 xv[8][2];
;     ...
; #pragma unroll
;         for (int j = 0; j < XPF; ++j) RESID_LD(j);
; #pragma unroll
;         for (int j = 0; j < 8; ++j) { const int ai = j >> 2, m = j & 3; bf16_t* rowp = X + (size_t)(row0 + ai * HALF + m * 16) * D + col0;
;             if (j + XPF < 8) RESID_LD(j + XPF);
;             asm volatile("" ::: "memory");
; #pragma unroll
;             for (int bj = 0; bj < 2; ++bj) { const u32x4 x = xv[j][bj];
;                 const f32x4 x0 = (f32x4){bf_lo(x.x), bf_hi(x.x), bf_lo(x.y), bf_hi(x.y)}, x1 = (f32x4){bf_lo(x.z), bf_hi(x.z), bf_lo(x.w), bf_hi(x.w)};
;                 const f32x4 r0 = acc[ai][bj][m][0] * gv[bj][0] + x0, r1 = acc[ai][bj][m][1] * gv[bj][1] + x1;
;                 u32x4 w; w.x = cvt_pk_bf16(r0[0], r0[1]); w.y = cvt_pk_bf16(r0[2], r0[3]); w.z = cvt_pk_bf16(r1[0], r1[1]); w.w = cvt_pk_bf16(r1[2], r1[3]);
;                 *(GAS u32x4*)(rowp + bj * HALF) = w; } }
.LBB0_1085:
	s_lshr_b32 s3, s2, 3
	s_cmpk_lt_i32 s2, 0x80
	s_mulk_i32 s3, 0x1800
	v_lshl_add_u32 v10, s2, 8, v1
	s_cselect_b32 s2, s3, 0x18000
	v_lshl_or_b32 v2, s6, 8, v214
	s_ashr_i32 s3, s2, 31
	v_ashrrev_i32_e32 v3, 31, v2
	v_readlane_b32 s8, v252, 20
	s_lshl_b64 s[2:3], s[2:3], 2
	v_lshlrev_b64 v[182:183], 1, v[2:3]
	v_readlane_b32 s9, v252, 21
	v_ashrrev_i32_e32 v11, 31, v10
	s_add_u32 s2, s46, s2
	v_lshl_add_u64 v[4:5], s[8:9], 0, v[182:183]
	v_lshlrev_b64 v[6:7], 11, v[10:11]
	s_addc_u32 s3, s47, s3
	s_nop 15
	v_lshl_add_u64 v[8:9], v[4:5], 0, v[6:7]
	v_lshl_add_u64 v[2:3], v[2:3], 2, s[2:3]
	s_mov_b64 s[2:3], 0x2000
	global_load_dwordx4 v[18:21], v[8:9], off
	global_load_dwordx4 v[216:219], v[8:9], off offset:256
	v_lshl_add_u64 v[8:9], v[2:3], 0, s[2:3]
	s_movk_i32 s2, 0x2000
	v_add_co_u32_e32 v2, vcc, s2, v2
	global_load_dwordx4 v[184:187], v[8:9], off offset:16
	global_load_dwordx4 v[220:223], v[8:9], off offset:512
	v_addc_co_u32_e32 v3, vcc, 0, v3, vcc
	global_load_dwordx4 v[224:227], v[8:9], off offset:528
	global_load_dwordx4 v[228:231], v[2:3], off
	v_or_b32_e32 v2, 16, v10
	v_ashrrev_i32_e32 v3, 31, v2
	v_lshlrev_b64 v[208:209], 11, v[2:3]
	v_lshl_add_u64 v[2:3], v[4:5], 0, v[208:209]
	global_load_dwordx4 v[232:235], v[2:3], off
	v_or_b32_e32 v12, 48, v10
	v_or_b32_e32 v8, 32, v10
	v_add_u32_e32 v14, 0x90, v10
	v_add_u32_e32 v16, 0xa0, v10
	v_ashrrev_i32_e32 v13, 31, v12
	s_mov_b64 s[2:3], 0x40000
	v_ashrrev_i32_e32 v9, 31, v8
	v_ashrrev_i32_e32 v15, 31, v14
	v_ashrrev_i32_e32 v17, 31, v16
	v_lshlrev_b64 v[204:205], 11, v[12:13]
	v_lshl_add_u64 v[202:203], v[6:7], 0, s[2:3]
	v_lshlrev_b64 v[206:207], 11, v[8:9]
	v_lshlrev_b64 v[200:201], 11, v[14:15]
	v_lshlrev_b64 v[8:9], 11, v[16:17]
	v_lshl_add_u64 v[14:15], v[4:5], 0, v[204:205]
	v_lshl_add_u64 v[16:17], v[4:5], 0, v[202:203]
	v_lshl_add_u64 v[12:13], v[4:5], 0, v[206:207]
	v_lshl_add_u64 v[4:5], v[4:5], 0, v[200:201]
	global_load_dwordx4 v[236:239], v[2:3], off offset:256
	global_load_dwordx4 v[174:177], v[12:13], off
	global_load_dwordx4 v[170:173], v[12:13], off offset:256
	global_load_dwordx4 v[166:169], v[14:15], off
	global_load_dwordx4 v[162:165], v[14:15], off offset:256
	global_load_dwordx4 v[30:33], v[16:17], off
	global_load_dwordx4 v[26:29], v[16:17], off offset:256
	global_load_dwordx4 v[22:25], v[4:5], off
	s_nop 0
	global_load_dwordx4 v[14:17], v[4:5], off offset:256
	v_lshl_add_u64 v[6:7], s[8:9], 0, v[6:7]
	v_lshl_add_u64 v[240:241], v[6:7], 0, v[182:183]
	v_lshl_add_u64 v[6:7], s[8:9], 0, v[8:9]
	v_lshl_add_u64 v[180:181], v[6:7], 0, v[182:183]
	s_mov_b32 s2, 0x38800000
	global_load_dwordx4 v[6:9], v[180:181], off
	global_load_dwordx4 v[2:5], v[180:181], off offset:256
	v_add_u32_e32 v10, 0xb0, v10
	v_ashrrev_i32_e32 v11, 31, v10
	v_lshlrev_b64 v[10:11], 11, v[10:11]
	v_lshl_add_u64 v[10:11], s[8:9], 0, v[10:11]
	s_andn2_b64 vcc, exec, s[36:37]
	s_waitcnt vmcnt(0)
	v_lshlrev_b32_e32 v242, 16, v20
	v_and_b32_e32 v243, 0xffff0000, v20
	v_lshlrev_b32_e32 v20, 16, v21
	v_and_b32_e32 v21, 0xffff0000, v21
	v_lshlrev_b32_e32 v12, 16, v18
	v_pk_mul_f32 v[198:199], v[186:187], s[2:3] op_sel_hi:[1,0]
	v_pk_mul_f32 v[196:197], v[184:185], s[2:3] op_sel_hi:[1,0]
	v_and_b32_e32 v13, 0xffff0000, v18
	v_lshlrev_b32_e32 v18, 16, v19
	v_and_b32_e32 v19, 0xffff0000, v19
	v_pk_mul_f32 v[188:189], v[220:221], s[2:3] op_sel_hi:[1,0]
	v_pk_fma_f32 v[220:221], v[152:153], v[198:199], v[20:21]
	v_pk_fma_f32 v[20:21], v[150:151], v[196:197], v[242:243]
	v_pk_mul_f32 v[152:153], v[230:231], s[2:3] op_sel_hi:[1,0]
	v_pk_mul_f32 v[150:151], v[228:229], s[2:3] op_sel_hi:[1,0]
	v_pk_fma_f32 v[148:149], v[148:149], v[152:153], v[18:19]
	v_pk_fma_f32 v[12:13], v[146:147], v[150:151], v[12:13]
	v_lshlrev_b32_e32 v244, 16, v216
	v_cvt_pk_bf16_f32 v18, v12, v13
	v_cvt_pk_bf16_f32 v19, v148, v149
	v_cvt_pk_bf16_f32 v20, v20, v21
	v_cvt_pk_bf16_f32 v21, v220, v221
	v_and_b32_e32 v245, 0xffff0000, v216
	v_pk_mul_f32 v[194:195], v[222:223], s[2:3] op_sel_hi:[1,0]
	v_pk_mul_f32 v[186:187], v[226:227], s[2:3] op_sel_hi:[1,0]
	v_pk_mul_f32 v[184:185], v[224:225], s[2:3] op_sel_hi:[1,0]
	global_store_dwordx4 v[240:241], v[18:21], off
	v_lshlrev_b32_e32 v12, 16, v217
	v_and_b32_e32 v13, 0xffff0000, v217
	v_lshlrev_b32_e32 v18, 16, v218
	v_and_b32_e32 v19, 0xffff0000, v218
	v_lshlrev_b32_e32 v20, 16, v219
	v_and_b32_e32 v21, 0xffff0000, v219
	v_pk_fma_f32 v[12:13], v[156:157], v[194:195], v[12:13]
	v_pk_fma_f32 v[146:147], v[154:155], v[188:189], v[244:245]
	v_pk_fma_f32 v[148:149], v[160:161], v[186:187], v[20:21]
	v_pk_fma_f32 v[20:21], v[158:159], v[184:185], v[18:19]
	v_cvt_pk_bf16_f32 v18, v146, v147
	v_cvt_pk_bf16_f32 v19, v12, v13
	v_lshl_add_u64 v[12:13], s[8:9], 0, v[208:209]
	v_cvt_pk_bf16_f32 v20, v20, v21
	v_cvt_pk_bf16_f32 v21, v148, v149
	global_store_dwordx4 v[240:241], v[18:21], off offset:256
	v_lshl_add_u64 v[146:147], v[10:11], 0, v[182:183]
	v_lshl_add_u64 v[148:149], v[12:13], 0, v[182:183]
	global_load_dwordx4 v[18:21], v[146:147], off
	global_load_dwordx4 v[10:13], v[146:147], off offset:256
	v_lshlrev_b32_e32 v154, 16, v232
	v_and_b32_e32 v155, 0xffff0000, v232
	v_lshlrev_b32_e32 v158, 16, v234
	v_and_b32_e32 v159, 0xffff0000, v234
	v_lshlrev_b32_e32 v160, 16, v235
	v_and_b32_e32 v161, 0xffff0000, v235
	v_lshlrev_b32_e32 v156, 16, v233
	v_and_b32_e32 v157, 0xffff0000, v233
	v_pk_fma_f32 v[138:139], v[138:139], v[150:151], v[154:155]
	v_pk_fma_f32 v[154:155], v[132:133], v[198:199], v[160:161]
	v_pk_fma_f32 v[132:133], v[130:131], v[196:197], v[158:159]
	v_pk_fma_f32 v[140:141], v[140:141], v[152:153], v[156:157]
	v_cvt_pk_bf16_f32 v130, v138, v139
	v_lshlrev_b32_e32 v138, 16, v238
; #define GAS __attribute__((address_space(1)))
; __device__ __forceinline__ unsigned cvt_pk_bf16(float lo, float hi) { unsigned r; asm volatile("v_cvt_pk_bf16_f32 %0, %1, %2" : "=v"(r) : "v"(lo), "v"(hi)); return r; }
; #define RESID_LD(j) do { _Pragma("unroll") for (int bj = 0; bj < 2; ++bj) xv[j][bj] = *(const GAS u32x4*)(X + (size_t)(row0 + ((j) >> 2) * HALF + ((j) & 3) * 16) * D + col0 + bj * HALF); } while (0)
;     __device__ __forceinline__ void operator()(const f32x4 (&acc)[2][2][4][2], const Unit& u, int wr, int wc, int fr, int fq) const {
;     ...
;         for (int j = 0; j < 8; ++j) { const int ai = j >> 2, m = j & 3; bf16_t* rowp = X + (size_t)(row0 + ai * HALF + m * 16) * D + col0;
;             if (j + XPF < 8) RESID_LD(j + XPF);
;             asm volatile("" ::: "memory");
; #pragma unroll
;             for (int bj = 0; bj < 2; ++bj) { const u32x4 x = xv[j][bj];
;                 const f32x4 x0 = (f32x4){bf_lo(x.x), bf_hi(x.x), bf_lo(x.y), bf_hi(x.y)}, x1 = (f32x4){bf_lo(x.z), bf_hi(x.z), bf_lo(x.w), bf_hi(x.w)};
;                 const f32x4 r0 = acc[ai][bj][m][0] * gv[bj][0] + x0, r1 = acc[ai][bj][m][1] * gv[bj][1] + x1;
;                 u32x4 w; w.x = cvt_pk_bf16(r0[0], r0[1]); w.y = cvt_pk_bf16(r0[2], r0[3]); w.z = cvt_pk_bf16(r1[0], r1[1]); w.w = cvt_pk_bf16(r1[2], r1[3]);
;                 *(GAS u32x4*)(rowp + bj * HALF) = w; } }
	v_cvt_pk_bf16_f32 v131, v140, v141
	v_cvt_pk_bf16_f32 v132, v132, v133
	v_cvt_pk_bf16_f32 v133, v154, v155
	global_store_dwordx4 v[148:149], v[130:133], off
	v_and_b32_e32 v139, 0xffff0000, v238
	v_lshlrev_b32_e32 v140, 16, v239
	v_lshlrev_b32_e32 v130, 16, v236
	v_and_b32_e32 v131, 0xffff0000, v236
	v_lshlrev_b32_e32 v132, 16, v237
	v_and_b32_e32 v133, 0xffff0000, v237
	v_and_b32_e32 v141, 0xffff0000, v239
	v_pk_fma_f32 v[132:133], v[144:145], v[194:195], v[132:133]
	v_pk_fma_f32 v[130:131], v[142:143], v[188:189], v[130:131]
	v_pk_fma_f32 v[136:137], v[136:137], v[186:187], v[140:141]
	v_pk_fma_f32 v[134:135], v[134:135], v[184:185], v[138:139]
	v_cvt_pk_bf16_f32 v130, v130, v131
	v_cvt_pk_bf16_f32 v131, v132, v133
	v_lshlrev_b32_e32 v138, 16, v177
	v_cvt_pk_bf16_f32 v132, v134, v135
	v_cvt_pk_bf16_f32 v133, v136, v137
	global_store_dwordx4 v[148:149], v[130:133], off offset:256
	v_lshlrev_b32_e32 v134, 16, v175
	v_and_b32_e32 v135, 0xffff0000, v175
	v_lshl_add_u64 v[130:131], s[8:9], 0, v[206:207]
	v_lshlrev_b32_e32 v132, 16, v174
	v_and_b32_e32 v133, 0xffff0000, v174
	v_lshlrev_b32_e32 v136, 16, v176
	v_and_b32_e32 v137, 0xffff0000, v176
	v_and_b32_e32 v139, 0xffff0000, v177
	v_lshl_add_u64 v[130:131], v[130:131], 0, v[182:183]
	v_pk_fma_f32 v[128:129], v[128:129], v[152:153], v[134:135]
	v_pk_fma_f32 v[126:127], v[126:127], v[150:151], v[132:133]
	v_pk_fma_f32 v[132:133], v[120:121], v[198:199], v[138:139]
	v_pk_fma_f32 v[120:121], v[118:119], v[196:197], v[136:137]
	v_cvt_pk_bf16_f32 v118, v126, v127
	v_cvt_pk_bf16_f32 v119, v128, v129
	v_lshlrev_b32_e32 v126, 16, v172
	v_cvt_pk_bf16_f32 v120, v120, v121
	v_cvt_pk_bf16_f32 v121, v132, v133
	global_store_dwordx4 v[130:131], v[118:121], off
	v_and_b32_e32 v127, 0xffff0000, v172
	v_lshlrev_b32_e32 v128, 16, v173
	v_lshlrev_b32_e32 v118, 16, v170
	v_and_b32_e32 v119, 0xffff0000, v170
	v_and_b32_e32 v129, 0xffff0000, v173
	v_lshlrev_b32_e32 v120, 16, v171
	v_and_b32_e32 v121, 0xffff0000, v171
	v_pk_fma_f32 v[118:119], v[122:123], v[188:189], v[118:119]
	v_pk_fma_f32 v[122:123], v[116:117], v[186:187], v[128:129]
	v_pk_fma_f32 v[116:117], v[114:115], v[184:185], v[126:127]
	v_pk_fma_f32 v[120:121], v[124:125], v[194:195], v[120:121]
	v_cvt_pk_bf16_f32 v114, v118, v119
	v_lshlrev_b32_e32 v118, 16, v167
	v_cvt_pk_bf16_f32 v115, v120, v121
	v_cvt_pk_bf16_f32 v116, v116, v117
	v_cvt_pk_bf16_f32 v117, v122, v123
	global_store_dwordx4 v[130:131], v[114:117], off offset:256
	v_and_b32_e32 v119, 0xffff0000, v167
	v_lshlrev_b32_e32 v120, 16, v168
	v_lshl_add_u64 v[114:115], s[8:9], 0, v[204:205]
	v_lshlrev_b32_e32 v116, 16, v166
	v_and_b32_e32 v117, 0xffff0000, v166
	v_and_b32_e32 v121, 0xffff0000, v168
	v_lshlrev_b32_e32 v122, 16, v169
	v_and_b32_e32 v123, 0xffff0000, v169
	v_lshl_add_u64 v[114:115], v[114:115], 0, v[182:183]
	v_pk_fma_f32 v[108:109], v[108:109], v[152:153], v[118:119]
	v_pk_fma_f32 v[106:107], v[106:107], v[150:151], v[116:117]
	v_pk_fma_f32 v[116:117], v[96:97], v[198:199], v[122:123]
	v_pk_fma_f32 v[96:97], v[94:95], v[196:197], v[120:121]
	v_cvt_pk_bf16_f32 v94, v106, v107
	v_cvt_pk_bf16_f32 v95, v108, v109
	v_lshlrev_b32_e32 v106, 16, v164
	v_cvt_pk_bf16_f32 v96, v96, v97
	v_cvt_pk_bf16_f32 v97, v116, v117
	global_store_dwordx4 v[114:115], v[94:97], off
	v_and_b32_e32 v107, 0xffff0000, v164
	v_lshlrev_b32_e32 v108, 16, v165
	v_lshlrev_b32_e32 v94, 16, v162
	v_and_b32_e32 v95, 0xffff0000, v162
	v_and_b32_e32 v109, 0xffff0000, v165
	v_lshlrev_b32_e32 v96, 16, v163
	v_and_b32_e32 v97, 0xffff0000, v163
	v_pk_fma_f32 v[86:87], v[86:87], v[188:189], v[94:95]
	v_pk_fma_f32 v[94:95], v[84:85], v[186:187], v[108:109]
	v_pk_fma_f32 v[84:85], v[82:83], v[184:185], v[106:107]
	v_pk_fma_f32 v[88:89], v[88:89], v[194:195], v[96:97]
	v_cvt_pk_bf16_f32 v82, v86, v87
	v_lshlrev_b32_e32 v86, 16, v32
	v_cvt_pk_bf16_f32 v83, v88, v89
	v_cvt_pk_bf16_f32 v84, v84, v85
	v_cvt_pk_bf16_f32 v85, v94, v95
	global_store_dwordx4 v[114:115], v[82:85], off offset:256
	v_and_b32_e32 v87, 0xffff0000, v32
	v_lshlrev_b32_e32 v32, 16, v33
	v_lshlrev_b32_e32 v84, 16, v30
	v_and_b32_e32 v85, 0xffff0000, v30
	v_lshlrev_b32_e32 v30, 16, v31
	v_and_b32_e32 v31, 0xffff0000, v31
	v_and_b32_e32 v33, 0xffff0000, v33
	v_lshl_add_u64 v[82:83], s[8:9], 0, v[202:203]
	v_pk_fma_f32 v[88:89], v[112:113], v[152:153], v[30:31]
	v_pk_fma_f32 v[30:31], v[110:111], v[150:151], v[84:85]
	v_pk_fma_f32 v[84:85], v[100:101], v[198:199], v[32:33]
	v_pk_fma_f32 v[32:33], v[98:99], v[196:197], v[86:87]
	v_lshl_add_u64 v[82:83], v[82:83], 0, v[182:183]
	v_cvt_pk_bf16_f32 v30, v30, v31
	v_cvt_pk_bf16_f32 v31, v88, v89
	v_cvt_pk_bf16_f32 v32, v32, v33
	v_cvt_pk_bf16_f32 v33, v84, v85
	global_store_dwordx4 v[82:83], v[30:33], off
	s_mov_b64 s[2:3], -1
	s_nop 0
	v_lshlrev_b32_e32 v30, 16, v26
	v_and_b32_e32 v31, 0xffff0000, v26
	v_lshlrev_b32_e32 v26, 16, v27
; #define GAS __attribute__((address_space(1)))
; __device__ __forceinline__ unsigned cvt_pk_bf16(float lo, float hi) { unsigned r; asm volatile("v_cvt_pk_bf16_f32 %0, %1, %2" : "=v"(r) : "v"(lo), "v"(hi)); return r; }
; #define PG8_BAR __builtin_amdgcn_s_barrier()
; #define RESID_LD(j) do { _Pragma("unroll") for (int bj = 0; bj < 2; ++bj) xv[j][bj] = *(const GAS u32x4*)(X + (size_t)(row0 + ((j) >> 2) * HALF + ((j) & 3) * 16) * D + col0 + bj * HALF); } while (0)
;     ...
;         E(acc, cur, wr, wc, fr, fq);
;         if (!has_next) break;
;         cur = nxt; cA = nA; cB = nB; ++ui;
; #pragma unroll
;         for (int _h = 0; _h < 2; ++_h)
; #pragma unroll
;             for (int _i = 0; _i < 2; ++_i) cvo[_h][_i] = nvo[_h][_i];
;         if constexpr (ALIGN_EPI) { if (wr == 1) PG8_BAR; }
;     __device__ __forceinline__ void operator()(const f32x4 (&acc)[2][2][4][2], const Unit& u, int wr, int wc, int fr, int fq) const {
;     ...
;         for (int j = 0; j < 8; ++j) { const int ai = j >> 2, m = j & 3; bf16_t* rowp = X + (size_t)(row0 + ai * HALF + m * 16) * D + col0;
;             if (j + XPF < 8) RESID_LD(j + XPF);
;             asm volatile("" ::: "memory");
; #pragma unroll
;             for (int bj = 0; bj < 2; ++bj) { const u32x4 x = xv[j][bj];
;                 const f32x4 x0 = (f32x4){bf_lo(x.x), bf_hi(x.x), bf_lo(x.y), bf_hi(x.y)}, x1 = (f32x4){bf_lo(x.z), bf_hi(x.z), bf_lo(x.w), bf_hi(x.w)};
;                 const f32x4 r0 = acc[ai][bj][m][0] * gv[bj][0] + x0, r1 = acc[ai][bj][m][1] * gv[bj][1] + x1;
;                 u32x4 w; w.x = cvt_pk_bf16(r0[0], r0[1]); w.y = cvt_pk_bf16(r0[2], r0[3]); w.z = cvt_pk_bf16(r1[0], r1[1]); w.w = cvt_pk_bf16(r1[2], r1[3]);
;                 *(GAS u32x4*)(rowp + bj * HALF) = w; } }
	v_and_b32_e32 v27, 0xffff0000, v27
	v_lshlrev_b32_e32 v32, 16, v28
	v_and_b32_e32 v33, 0xffff0000, v28
	v_lshlrev_b32_e32 v28, 16, v29
	v_and_b32_e32 v29, 0xffff0000, v29
	v_pk_fma_f32 v[84:85], v[104:105], v[194:195], v[26:27]
	v_pk_fma_f32 v[26:27], v[102:103], v[188:189], v[30:31]
	v_pk_fma_f32 v[30:31], v[92:93], v[186:187], v[28:29]
	v_pk_fma_f32 v[28:29], v[90:91], v[184:185], v[32:33]
	v_cvt_pk_bf16_f32 v26, v26, v27
	v_cvt_pk_bf16_f32 v27, v84, v85
	s_nop 0
	v_cvt_pk_bf16_f32 v28, v28, v29
	v_cvt_pk_bf16_f32 v29, v30, v31
	global_store_dwordx4 v[82:83], v[26:29], off offset:256
	v_lshlrev_b32_e32 v30, 16, v24
	v_and_b32_e32 v31, 0xffff0000, v24
	v_lshlrev_b32_e32 v28, 16, v22
	v_and_b32_e32 v29, 0xffff0000, v22
	v_lshlrev_b32_e32 v22, 16, v23
	v_and_b32_e32 v23, 0xffff0000, v23
	v_lshlrev_b32_e32 v24, 16, v25
	v_and_b32_e32 v25, 0xffff0000, v25
	v_lshl_add_u64 v[26:27], s[8:9], 0, v[200:201]
	v_pk_fma_f32 v[32:33], v[80:81], v[152:153], v[22:23]
	v_pk_fma_f32 v[22:23], v[78:79], v[150:151], v[28:29]
	v_pk_fma_f32 v[28:29], v[76:77], v[198:199], v[24:25]
	v_pk_fma_f32 v[24:25], v[74:75], v[196:197], v[30:31]
	v_lshl_add_u64 v[26:27], v[26:27], 0, v[182:183]
	v_cvt_pk_bf16_f32 v22, v22, v23
	v_cvt_pk_bf16_f32 v23, v32, v33
	v_cvt_pk_bf16_f32 v24, v24, v25
	v_cvt_pk_bf16_f32 v25, v28, v29
	global_store_dwordx4 v[26:27], v[22:25], off
	s_nop 1
	v_lshlrev_b32_e32 v22, 16, v14
	v_and_b32_e32 v23, 0xffff0000, v14
	v_lshlrev_b32_e32 v14, 16, v15
	v_and_b32_e32 v15, 0xffff0000, v15
	v_lshlrev_b32_e32 v24, 16, v16
	v_and_b32_e32 v25, 0xffff0000, v16
	v_lshlrev_b32_e32 v16, 16, v17
	v_and_b32_e32 v17, 0xffff0000, v17
	v_pk_fma_f32 v[28:29], v[72:73], v[194:195], v[14:15]
	v_pk_fma_f32 v[14:15], v[70:71], v[188:189], v[22:23]
	v_pk_fma_f32 v[22:23], v[68:69], v[186:187], v[16:17]
	v_pk_fma_f32 v[16:17], v[66:67], v[184:185], v[24:25]
	v_cvt_pk_bf16_f32 v14, v14, v15
	v_cvt_pk_bf16_f32 v15, v28, v29
	s_nop 0
	v_cvt_pk_bf16_f32 v16, v16, v17
	v_cvt_pk_bf16_f32 v17, v22, v23
	global_store_dwordx4 v[26:27], v[14:17], off offset:256
	s_nop 1
	v_lshlrev_b32_e32 v14, 16, v6
	v_and_b32_e32 v15, 0xffff0000, v6
	v_lshlrev_b32_e32 v6, 16, v7
	v_and_b32_e32 v7, 0xffff0000, v7
	v_lshlrev_b32_e32 v16, 16, v8
	v_and_b32_e32 v17, 0xffff0000, v8
	v_lshlrev_b32_e32 v8, 16, v9
	v_and_b32_e32 v9, 0xffff0000, v9
	v_pk_fma_f32 v[22:23], v[64:65], v[152:153], v[6:7]
	v_pk_fma_f32 v[6:7], v[62:63], v[150:151], v[14:15]
	v_pk_fma_f32 v[14:15], v[60:61], v[198:199], v[8:9]
	v_pk_fma_f32 v[8:9], v[58:59], v[196:197], v[16:17]
	v_cvt_pk_bf16_f32 v6, v6, v7
	v_cvt_pk_bf16_f32 v7, v22, v23
	s_nop 0
	v_cvt_pk_bf16_f32 v8, v8, v9
	v_cvt_pk_bf16_f32 v9, v14, v15
	global_store_dwordx4 v[180:181], v[6:9], off
	s_nop 1
	v_lshlrev_b32_e32 v6, 16, v2
	v_and_b32_e32 v7, 0xffff0000, v2
	v_lshlrev_b32_e32 v2, 16, v3
	v_and_b32_e32 v3, 0xffff0000, v3
	v_lshlrev_b32_e32 v8, 16, v4
	v_and_b32_e32 v9, 0xffff0000, v4
	v_lshlrev_b32_e32 v4, 16, v5
	v_and_b32_e32 v5, 0xffff0000, v5
	v_pk_fma_f32 v[14:15], v[56:57], v[194:195], v[2:3]
	v_pk_fma_f32 v[2:3], v[54:55], v[188:189], v[6:7]
	v_pk_fma_f32 v[6:7], v[52:53], v[186:187], v[4:5]
	v_pk_fma_f32 v[4:5], v[50:51], v[184:185], v[8:9]
	v_cvt_pk_bf16_f32 v2, v2, v3
	v_cvt_pk_bf16_f32 v3, v14, v15
	s_waitcnt vmcnt(12)
	v_lshlrev_b32_e32 v8, 16, v21
	v_cvt_pk_bf16_f32 v4, v4, v5
	v_cvt_pk_bf16_f32 v5, v6, v7
	global_store_dwordx4 v[180:181], v[2:5], off offset:256
	v_lshlrev_b32_e32 v6, 16, v20
	v_and_b32_e32 v7, 0xffff0000, v20
	v_lshlrev_b32_e32 v2, 16, v18
	v_and_b32_e32 v3, 0xffff0000, v18
	v_lshlrev_b32_e32 v4, 16, v19
	v_and_b32_e32 v5, 0xffff0000, v19
	v_and_b32_e32 v9, 0xffff0000, v21
	v_pk_fma_f32 v[4:5], v[48:49], v[152:153], v[4:5]
	v_pk_fma_f32 v[2:3], v[46:47], v[150:151], v[2:3]
	v_pk_fma_f32 v[8:9], v[44:45], v[198:199], v[8:9]
	v_pk_fma_f32 v[6:7], v[42:43], v[196:197], v[6:7]
	v_cvt_pk_bf16_f32 v2, v2, v3
	v_cvt_pk_bf16_f32 v3, v4, v5
	s_nop 0
	v_cvt_pk_bf16_f32 v4, v6, v7
	v_cvt_pk_bf16_f32 v5, v8, v9
	global_store_dwordx4 v[146:147], v[2:5], off
	s_waitcnt vmcnt(13)
	v_lshlrev_b32_e32 v6, 16, v12
	v_and_b32_e32 v7, 0xffff0000, v12
	v_lshlrev_b32_e32 v2, 16, v10
	v_and_b32_e32 v3, 0xffff0000, v10
	v_lshlrev_b32_e32 v4, 16, v11
	v_and_b32_e32 v5, 0xffff0000, v11
	v_lshlrev_b32_e32 v8, 16, v13
	v_and_b32_e32 v9, 0xffff0000, v13
	v_pk_fma_f32 v[4:5], v[40:41], v[194:195], v[4:5]
	v_pk_fma_f32 v[2:3], v[38:39], v[188:189], v[2:3]
	v_pk_fma_f32 v[8:9], v[36:37], v[186:187], v[8:9]
	v_pk_fma_f32 v[6:7], v[34:35], v[184:185], v[6:7]
	v_cvt_pk_bf16_f32 v2, v2, v3
	v_cvt_pk_bf16_f32 v3, v4, v5
	s_nop 0
	v_cvt_pk_bf16_f32 v4, v6, v7
	v_cvt_pk_bf16_f32 v5, v8, v9
	global_store_dwordx4 v[146:147], v[2:5], off offset:256
	s_cbranch_vccnz .LBB0_1078
	s_andn2_b64 vcc, exec, s[0:1]
	s_cbranch_vccnz .LBB0_1077
	s_barrier
	s_branch .LBB0_1077

;     ...
;         if constexpr (FP8) { asm volatile("s_nop 15\n\ts_nop 15\n\ts_nop 15\n\ts_nop 15" ::: "memory"); }
;     __device__ __forceinline__ void operator()(const f32x4 (&acc)[2][2][4][2], const Unit& u, int wr, int wc, int fr, int fq) const {
;         const int row0 = u.pm * BM + wr * 64 + fr, col0 = (u.pn & 7) * 128 + wc * 32 + 8 * fq;
;         constexpr float ds = 1.0f / (SC_W * SC_H2);
;         constexpr float c1 = -ds * LOG2E, kk = 1.0f / (ds * ds * SC_HID);
; #pragma unroll
;         for (int ai = 0; ai < 2; ++ai)
; #pragma unroll
;             for (int m = 0; m < 4; ++m) { unsigned char* rowp = HID8 + (size_t)(row0 + ai * HALF + m * 16) * D + col0;
;                 const f32x4 g0 = acc[ai][0][m][0], g1 = acc[ai][0][m][1], u0 = acc[ai][1][m][0], u1 = acc[ai][1][m][1];
;                 f32x4 t0 = g0 * c1, t1 = g1 * c1;
; #pragma unroll
;                 for (int e = 0; e < 4; ++e) { t0[e] = __builtin_amdgcn_exp2f(t0[e]); t1[e] = __builtin_amdgcn_exp2f(t1[e]); }
;                 f32x4 d0 = t0 * kk + kk, d1 = t1 * kk + kk;
; #pragma unroll
;                 for (int e = 0; e < 4; ++e) { d0[e] = __builtin_amdgcn_rcpf(d0[e]); d1[e] = __builtin_amdgcn_rcpf(d1[e]); }
;                 const f32x4 v0 = (g0 * u0) * d0, v1 = (g1 * u1) * d1;
;                 u32x2 w; w.x = pack4_fp8(v0[0], v0[1], v0[2], v0[3]); w.y = pack4_fp8(v1[0], v1[1], v1[2], v1[3]);
;                 *(u32x2*)rowp = w; }
.LBB0_1427:
	v_pk_mul_f32 v[2:3], v[152:153], s[24:25] op_sel_hi:[1,0]
	v_pk_mul_f32 v[6:7], v[150:151], s[24:25] op_sel_hi:[1,0]
	v_pk_mul_f32 v[8:9], v[148:149], s[24:25] op_sel_hi:[1,0]
	v_exp_f32_e32 v6, v6
	v_exp_f32_e32 v7, v7
	v_exp_f32_e32 v2, v2
	v_exp_f32_e32 v3, v3
	v_exp_f32_e32 v8, v8
	v_exp_f32_e32 v9, v9
	v_pk_mul_f32 v[10:11], v[146:147], s[24:25] op_sel_hi:[1,0]
	v_pk_fma_f32 v[2:3], v[2:3], s[26:27], s[26:27] op_sel_hi:[1,0,0]
	v_exp_f32_e32 v10, v10
	v_exp_f32_e32 v11, v11
	v_pk_fma_f32 v[6:7], v[6:7], s[26:27], s[26:27] op_sel_hi:[1,0,0]
	v_pk_fma_f32 v[8:9], v[8:9], s[26:27], s[26:27] op_sel_hi:[1,0,0]
	v_rcp_f32_e32 v6, v6
	v_rcp_f32_e32 v7, v7
	v_rcp_f32_e32 v2, v2
	v_rcp_f32_e32 v3, v3
	v_rcp_f32_e32 v8, v8
	v_rcp_f32_e32 v9, v9
	v_pk_fma_f32 v[10:11], v[10:11], s[26:27], s[26:27] op_sel_hi:[1,0,0]
	v_pk_mul_f32 v[12:13], v[152:153], v[160:161]
	v_rcp_f32_e32 v10, v10
	v_rcp_f32_e32 v11, v11
	v_pk_mul_f32 v[14:15], v[150:151], v[158:159]
	v_pk_mul_f32 v[2:3], v[12:13], v[2:3]
	v_pk_mul_f32 v[6:7], v[14:15], v[6:7]
	v_pk_mul_f32 v[12:13], v[148:149], v[156:157]
	v_med3_f32 v7, v7, s15, v212
	v_pk_mul_f32 v[8:9], v[12:13], v[8:9]
	v_med3_f32 v12, v6, s15, v212
	v_mov_b32_e32 v6, v191
	v_pk_mul_f32 v[14:15], v[146:147], v[154:155]
	v_cvt_pk_fp8_f32 v6, v12, v7
	v_pk_mul_f32 v[10:11], v[14:15], v[10:11]
	v_mov_b32_e32 v7, v191
	v_med3_f32 v10, v10, s15, v212
	v_med3_f32 v11, v11, s15, v212
	v_med3_f32 v2, v2, s15, v212
	v_med3_f32 v3, v3, s15, v212
	v_cvt_pk_fp8_f32 v7, v10, v11
	v_pk_mul_f32 v[10:11], v[134:135], s[24:25] op_sel_hi:[1,0]
	v_cvt_pk_fp8_f32 v6, v2, v3 op_sel:[0,0,1]
	v_med3_f32 v2, v8, s15, v212
	v_med3_f32 v3, v9, s15, v212
	v_pk_mul_f32 v[8:9], v[136:137], s[24:25] op_sel_hi:[1,0]
	v_pk_mul_f32 v[14:15], v[130:131], s[24:25] op_sel_hi:[1,0]
	v_exp_f32_e32 v10, v10
	v_exp_f32_e32 v11, v11
	v_exp_f32_e32 v14, v14
	v_exp_f32_e32 v8, v8
	v_exp_f32_e32 v9, v9
	v_exp_f32_e32 v15, v15
	v_pk_mul_f32 v[12:13], v[132:133], s[24:25] op_sel_hi:[1,0]
	v_pk_fma_f32 v[10:11], v[10:11], s[26:27], s[26:27] op_sel_hi:[1,0,0]
	v_exp_f32_e32 v12, v12
	v_exp_f32_e32 v13, v13
	v_pk_fma_f32 v[8:9], v[8:9], s[26:27], s[26:27] op_sel_hi:[1,0,0]
	v_pk_fma_f32 v[14:15], v[14:15], s[26:27], s[26:27] op_sel_hi:[1,0,0]
	v_rcp_f32_e32 v10, v10
	v_rcp_f32_e32 v11, v11
	v_rcp_f32_e32 v14, v14
	v_rcp_f32_e32 v15, v15
	v_rcp_f32_e32 v8, v8
	v_rcp_f32_e32 v9, v9
	v_lshl_add_u32 v4, s51, 8, v175
	v_pk_mul_f32 v[18:19], v[134:135], v[142:143]
	v_ashrrev_i32_e32 v5, 31, v4
	v_pk_fma_f32 v[12:13], v[12:13], s[26:27], s[26:27] op_sel_hi:[1,0,0]
	v_pk_mul_f32 v[16:17], v[136:137], v[144:145]
	v_pk_mul_f32 v[10:11], v[18:19], v[10:11]
	v_pk_mul_f32 v[18:19], v[130:131], v[138:139]
	v_cvt_pk_fp8_f32 v7, v2, v3 op_sel:[0,0,1]
	v_lshlrev_b64 v[2:3], 10, v[4:5]
	v_rcp_f32_e32 v12, v12
	v_rcp_f32_e32 v13, v13
	v_pk_mul_f32 v[8:9], v[16:17], v[8:9]
	v_pk_mul_f32 v[14:15], v[18:19], v[14:15]
	v_med3_f32 v5, v10, s15, v212
	v_med3_f32 v11, v11, s15, v212
	v_mov_b32_e32 v10, v191
	s_lshl_b32 s7, s50, 7
	v_readlane_b32 s10, v252, 13
	v_cvt_pk_fp8_f32 v10, v5, v11
	v_med3_f32 v5, v8, s15, v212
	v_med3_f32 v8, v9, s15, v212
	v_med3_f32 v9, v14, s15, v212
	v_med3_f32 v14, v15, s15, v212
	v_mov_b32_e32 v11, v191
	s_and_b32 s7, s7, 0x380
	v_readlane_b32 s11, v252, 14
	v_cvt_pk_fp8_f32 v11, v9, v14
	v_or_b32_e32 v190, s7, v169
	v_lshl_add_u64 v[2:3], s[10:11], 0, v[2:3]
	v_pk_mul_f32 v[16:17], v[132:133], v[140:141]
	v_lshl_add_u64 v[2:3], v[2:3], 0, v[190:191]
	v_pk_mul_f32 v[12:13], v[16:17], v[12:13]
	s_nop 15
	global_store_dwordx2 v[2:3], v[6:7], off
	v_or_b32_e32 v6, 16, v4
	v_cvt_pk_fp8_f32 v10, v5, v8 op_sel:[0,0,1]
	v_med3_f32 v5, v12, s15, v212
	v_med3_f32 v8, v13, s15, v212
	v_ashrrev_i32_e32 v7, 31, v6
	v_cvt_pk_fp8_f32 v11, v5, v8 op_sel:[0,0,1]
	v_lshlrev_b64 v[6:7], 10, v[6:7]
	v_lshl_add_u64 v[6:7], s[10:11], 0, v[6:7]
	v_lshl_add_u64 v[6:7], v[6:7], 0, v[190:191]
	global_store_dwordx2 v[6:7], v[10:11], off
	v_pk_mul_f32 v[10:11], v[118:119], s[24:25] op_sel_hi:[1,0]
	v_pk_mul_f32 v[8:9], v[120:121], s[24:25] op_sel_hi:[1,0]
	v_pk_mul_f32 v[14:15], v[114:115], s[24:25] op_sel_hi:[1,0]
	v_exp_f32_e32 v10, v10
	v_exp_f32_e32 v11, v11
	v_exp_f32_e32 v14, v14
	v_exp_f32_e32 v8, v8
	v_exp_f32_e32 v9, v9
	v_exp_f32_e32 v15, v15
	v_pk_mul_f32 v[12:13], v[116:117], s[24:25] op_sel_hi:[1,0]
	v_pk_fma_f32 v[10:11], v[10:11], s[26:27], s[26:27] op_sel_hi:[1,0,0]
	v_exp_f32_e32 v12, v12
	v_exp_f32_e32 v13, v13
	v_pk_fma_f32 v[8:9], v[8:9], s[26:27], s[26:27] op_sel_hi:[1,0,0]
	v_pk_fma_f32 v[14:15], v[14:15], s[26:27], s[26:27] op_sel_hi:[1,0,0]
	v_rcp_f32_e32 v10, v10
	v_rcp_f32_e32 v11, v11
	v_rcp_f32_e32 v14, v14
	v_rcp_f32_e32 v15, v15
	v_rcp_f32_e32 v8, v8
	v_rcp_f32_e32 v9, v9
	v_pk_mul_f32 v[18:19], v[118:119], v[126:127]
	v_pk_fma_f32 v[12:13], v[12:13], s[26:27], s[26:27] op_sel_hi:[1,0,0]
	v_pk_mul_f32 v[16:17], v[120:121], v[128:129]
	v_pk_mul_f32 v[10:11], v[18:19], v[10:11]
	v_pk_mul_f32 v[18:19], v[114:115], v[122:123]
	v_rcp_f32_e32 v12, v12
	v_rcp_f32_e32 v13, v13
	v_pk_mul_f32 v[8:9], v[16:17], v[8:9]
	v_pk_mul_f32 v[14:15], v[18:19], v[14:15]
	v_med3_f32 v5, v10, s15, v212
	v_med3_f32 v11, v11, s15, v212
	v_mov_b32_e32 v10, v191
	v_cvt_pk_fp8_f32 v10, v5, v11
	v_med3_f32 v5, v8, s15, v212
	v_med3_f32 v8, v9, s15, v212
	v_med3_f32 v9, v14, s15, v212
	v_med3_f32 v14, v15, s15, v212
	v_mov_b32_e32 v11, v191
	v_cvt_pk_fp8_f32 v11, v9, v14
	v_pk_mul_f32 v[16:17], v[116:117], v[124:125]
	v_or_b32_e32 v6, 32, v4
	v_pk_mul_f32 v[12:13], v[16:17], v[12:13]
	v_cvt_pk_fp8_f32 v10, v5, v8 op_sel:[0,0,1]
	v_med3_f32 v5, v12, s15, v212
;     __device__ __forceinline__ void operator()(const f32x4 (&acc)[2][2][4][2], const Unit& u, int wr, int wc, int fr, int fq) const {
;     ...
;             for (int m = 0; m < 4; ++m) { unsigned char* rowp = HID8 + (size_t)(row0 + ai * HALF + m * 16) * D + col0;
;                 const f32x4 g0 = acc[ai][0][m][0], g1 = acc[ai][0][m][1], u0 = acc[ai][1][m][0], u1 = acc[ai][1][m][1];
;                 f32x4 t0 = g0 * c1, t1 = g1 * c1;
; #pragma unroll
;                 for (int e = 0; e < 4; ++e) { t0[e] = __builtin_amdgcn_exp2f(t0[e]); t1[e] = __builtin_amdgcn_exp2f(t1[e]); }
;                 f32x4 d0 = t0 * kk + kk, d1 = t1 * kk + kk;
; #pragma unroll
;                 for (int e = 0; e < 4; ++e) { d0[e] = __builtin_amdgcn_rcpf(d0[e]); d1[e] = __builtin_amdgcn_rcpf(d1[e]); }
;                 const f32x4 v0 = (g0 * u0) * d0, v1 = (g1 * u1) * d1;
;                 u32x2 w; w.x = pack4_fp8(v0[0], v0[1], v0[2], v0[3]); w.y = pack4_fp8(v1[0], v1[1], v1[2], v1[3]);
;                 *(u32x2*)rowp = w; }
	v_med3_f32 v8, v13, s15, v212
	v_ashrrev_i32_e32 v7, 31, v6
	v_cvt_pk_fp8_f32 v11, v5, v8 op_sel:[0,0,1]
	v_lshlrev_b64 v[6:7], 10, v[6:7]
	v_lshl_add_u64 v[6:7], s[10:11], 0, v[6:7]
	v_lshl_add_u64 v[6:7], v[6:7], 0, v[190:191]
	global_store_dwordx2 v[6:7], v[10:11], off
	v_pk_mul_f32 v[6:7], v[92:93], s[24:25] op_sel_hi:[1,0]
	v_pk_mul_f32 v[8:9], v[90:91], s[24:25] op_sel_hi:[1,0]
	v_pk_mul_f32 v[10:11], v[84:85], s[24:25] op_sel_hi:[1,0]
	v_pk_mul_f32 v[12:13], v[82:83], s[24:25] op_sel_hi:[1,0]
	v_exp_f32_e32 v8, v8
	v_exp_f32_e32 v9, v9
	v_exp_f32_e32 v6, v6
	v_exp_f32_e32 v7, v7
	v_exp_f32_e32 v12, v12
	v_exp_f32_e32 v10, v10
	v_exp_f32_e32 v11, v11
	v_exp_f32_e32 v13, v13
	v_pk_fma_f32 v[6:7], v[6:7], s[26:27], s[26:27] op_sel_hi:[1,0,0]
	v_pk_fma_f32 v[8:9], v[8:9], s[26:27], s[26:27] op_sel_hi:[1,0,0]
	v_pk_fma_f32 v[10:11], v[10:11], s[26:27], s[26:27] op_sel_hi:[1,0,0]
	v_pk_fma_f32 v[12:13], v[12:13], s[26:27], s[26:27] op_sel_hi:[1,0,0]
	v_rcp_f32_e32 v8, v8
	v_rcp_f32_e32 v9, v9
	v_rcp_f32_e32 v6, v6
	v_rcp_f32_e32 v7, v7
	v_rcp_f32_e32 v12, v12
	v_rcp_f32_e32 v13, v13
	v_rcp_f32_e32 v10, v10
	v_rcp_f32_e32 v11, v11
	v_pk_mul_f32 v[14:15], v[92:93], v[104:105]
	v_pk_mul_f32 v[16:17], v[90:91], v[102:103]
	v_pk_mul_f32 v[6:7], v[14:15], v[6:7]
	v_pk_mul_f32 v[8:9], v[16:17], v[8:9]
	v_pk_mul_f32 v[14:15], v[84:85], v[100:101]
	v_pk_mul_f32 v[16:17], v[82:83], v[98:99]
	v_pk_mul_f32 v[10:11], v[14:15], v[10:11]
	v_pk_mul_f32 v[12:13], v[16:17], v[12:13]
	v_med3_f32 v14, v8, s15, v212
	v_med3_f32 v9, v9, s15, v212
	v_mov_b32_e32 v8, v191
	v_cvt_pk_fp8_f32 v8, v14, v9
	v_med3_f32 v12, v12, s15, v212
	v_med3_f32 v13, v13, s15, v212
	v_mov_b32_e32 v9, v191
	v_cvt_pk_fp8_f32 v9, v12, v13
	v_med3_f32 v6, v6, s15, v212
	v_med3_f32 v7, v7, s15, v212
	v_or_b32_e32 v4, 48, v4
	v_cvt_pk_fp8_f32 v8, v6, v7 op_sel:[0,0,1]
	v_med3_f32 v6, v10, s15, v212
	v_med3_f32 v7, v11, s15, v212
	v_ashrrev_i32_e32 v5, 31, v4
	v_cvt_pk_fp8_f32 v9, v6, v7 op_sel:[0,0,1]
	v_lshlrev_b64 v[4:5], 10, v[4:5]
	v_lshl_add_u64 v[4:5], s[10:11], 0, v[4:5]
	v_lshl_add_u64 v[4:5], v[4:5], 0, v[190:191]
	global_store_dwordx2 v[4:5], v[8:9], off
	v_pk_mul_f32 v[4:5], v[96:97], s[24:25] op_sel_hi:[1,0]
	v_pk_mul_f32 v[6:7], v[94:95], s[24:25] op_sel_hi:[1,0]
	v_pk_mul_f32 v[8:9], v[88:89], s[24:25] op_sel_hi:[1,0]
	v_pk_mul_f32 v[10:11], v[86:87], s[24:25] op_sel_hi:[1,0]
	v_exp_f32_e32 v6, v6
	v_exp_f32_e32 v7, v7
	v_exp_f32_e32 v4, v4
	v_exp_f32_e32 v5, v5
	v_exp_f32_e32 v10, v10
	v_exp_f32_e32 v8, v8
	v_exp_f32_e32 v9, v9
	v_exp_f32_e32 v11, v11
	v_pk_fma_f32 v[4:5], v[4:5], s[26:27], s[26:27] op_sel_hi:[1,0,0]
	v_pk_fma_f32 v[6:7], v[6:7], s[26:27], s[26:27] op_sel_hi:[1,0,0]
	v_pk_fma_f32 v[8:9], v[8:9], s[26:27], s[26:27] op_sel_hi:[1,0,0]
	v_pk_fma_f32 v[10:11], v[10:11], s[26:27], s[26:27] op_sel_hi:[1,0,0]
	v_rcp_f32_e32 v6, v6
	v_rcp_f32_e32 v7, v7
	v_rcp_f32_e32 v4, v4
	v_rcp_f32_e32 v5, v5
	v_rcp_f32_e32 v10, v10
	v_rcp_f32_e32 v11, v11
	v_rcp_f32_e32 v8, v8
	v_rcp_f32_e32 v9, v9
	v_pk_mul_f32 v[12:13], v[96:97], v[112:113]
	v_pk_mul_f32 v[14:15], v[94:95], v[110:111]
	v_pk_mul_f32 v[4:5], v[12:13], v[4:5]
	v_pk_mul_f32 v[6:7], v[14:15], v[6:7]
	v_pk_mul_f32 v[12:13], v[88:89], v[108:109]
	v_pk_mul_f32 v[14:15], v[86:87], v[106:107]
	v_pk_mul_f32 v[8:9], v[12:13], v[8:9]
	v_pk_mul_f32 v[10:11], v[14:15], v[10:11]
	v_med3_f32 v12, v6, s15, v212
	v_med3_f32 v7, v7, s15, v212
	v_mov_b32_e32 v6, v191
	v_cvt_pk_fp8_f32 v6, v12, v7
	v_med3_f32 v10, v10, s15, v212
	v_med3_f32 v11, v11, s15, v212
	v_mov_b32_e32 v7, v191
	v_cvt_pk_fp8_f32 v7, v10, v11
	v_med3_f32 v4, v4, s15, v212
	v_med3_f32 v5, v5, s15, v212
	v_cvt_pk_fp8_f32 v6, v4, v5 op_sel:[0,0,1]
	v_med3_f32 v4, v8, s15, v212
	v_med3_f32 v5, v9, s15, v212
	v_cvt_pk_fp8_f32 v7, v4, v5 op_sel:[0,0,1]
	s_mov_b32 s7, 0x20000
	v_add_co_u32_e32 v4, vcc, s7, v2
	v_pk_mul_f32 v[8:9], v[68:69], s[24:25] op_sel_hi:[1,0]
	s_nop 0
	v_addc_co_u32_e32 v5, vcc, 0, v3, vcc
	global_store_dwordx2 v[4:5], v[6:7], off
	v_pk_mul_f32 v[4:5], v[72:73], s[24:25] op_sel_hi:[1,0]
	v_pk_mul_f32 v[6:7], v[70:71], s[24:25] op_sel_hi:[1,0]
	v_pk_mul_f32 v[10:11], v[66:67], s[24:25] op_sel_hi:[1,0]
	v_exp_f32_e32 v6, v6
	v_exp_f32_e32 v7, v7
	v_exp_f32_e32 v4, v4
	v_exp_f32_e32 v5, v5
	v_exp_f32_e32 v10, v10
	v_exp_f32_e32 v8, v8
	v_exp_f32_e32 v9, v9
	v_exp_f32_e32 v11, v11
	v_pk_fma_f32 v[4:5], v[4:5], s[26:27], s[26:27] op_sel_hi:[1,0,0]
	v_pk_fma_f32 v[6:7], v[6:7], s[26:27], s[26:27] op_sel_hi:[1,0,0]
	v_pk_fma_f32 v[8:9], v[8:9], s[26:27], s[26:27] op_sel_hi:[1,0,0]
	v_pk_fma_f32 v[10:11], v[10:11], s[26:27], s[26:27] op_sel_hi:[1,0,0]
	v_rcp_f32_e32 v6, v6
	v_rcp_f32_e32 v7, v7
	v_rcp_f32_e32 v4, v4
	v_rcp_f32_e32 v5, v5
; #define PG8_BAR __builtin_amdgcn_s_barrier()
;     ...
;         E(acc, cur, wr, wc, fr, fq);
;         if (!has_next) break;
;         cur = nxt; cA = nA; cB = nB; ++ui;
; #pragma unroll
;         for (int _h = 0; _h < 2; ++_h)
; #pragma unroll
;             for (int _i = 0; _i < 2; ++_i) cvo[_h][_i] = nvo[_h][_i];
;         if constexpr (ALIGN_EPI) { if (wr == 1) PG8_BAR; }
;     __device__ __forceinline__ void operator()(const f32x4 (&acc)[2][2][4][2], const Unit& u, int wr, int wc, int fr, int fq) const {
;     ...
;             for (int m = 0; m < 4; ++m) { unsigned char* rowp = HID8 + (size_t)(row0 + ai * HALF + m * 16) * D + col0;
;                 const f32x4 g0 = acc[ai][0][m][0], g1 = acc[ai][0][m][1], u0 = acc[ai][1][m][0], u1 = acc[ai][1][m][1];
;                 f32x4 t0 = g0 * c1, t1 = g1 * c1;
; #pragma unroll
;                 for (int e = 0; e < 4; ++e) { t0[e] = __builtin_amdgcn_exp2f(t0[e]); t1[e] = __builtin_amdgcn_exp2f(t1[e]); }
;                 f32x4 d0 = t0 * kk + kk, d1 = t1 * kk + kk;
; #pragma unroll
;                 for (int e = 0; e < 4; ++e) { d0[e] = __builtin_amdgcn_rcpf(d0[e]); d1[e] = __builtin_amdgcn_rcpf(d1[e]); }
;                 const f32x4 v0 = (g0 * u0) * d0, v1 = (g1 * u1) * d1;
;                 u32x2 w; w.x = pack4_fp8(v0[0], v0[1], v0[2], v0[3]); w.y = pack4_fp8(v1[0], v1[1], v1[2], v1[3]);
;                 *(u32x2*)rowp = w; }
	v_rcp_f32_e32 v10, v10
	v_rcp_f32_e32 v11, v11
	v_rcp_f32_e32 v8, v8
	v_rcp_f32_e32 v9, v9
	v_pk_mul_f32 v[12:13], v[72:73], v[80:81]
	v_pk_mul_f32 v[14:15], v[70:71], v[78:79]
	v_pk_mul_f32 v[4:5], v[12:13], v[4:5]
	v_pk_mul_f32 v[6:7], v[14:15], v[6:7]
	v_pk_mul_f32 v[12:13], v[68:69], v[76:77]
	v_pk_mul_f32 v[14:15], v[66:67], v[74:75]
	v_pk_mul_f32 v[8:9], v[12:13], v[8:9]
	v_pk_mul_f32 v[10:11], v[14:15], v[10:11]
	v_med3_f32 v12, v6, s15, v212
	v_med3_f32 v7, v7, s15, v212
	v_mov_b32_e32 v6, v191
	v_cvt_pk_fp8_f32 v6, v12, v7
	v_med3_f32 v10, v10, s15, v212
	v_med3_f32 v11, v11, s15, v212
	v_mov_b32_e32 v7, v191
	v_cvt_pk_fp8_f32 v7, v10, v11
	v_med3_f32 v4, v4, s15, v212
	v_med3_f32 v5, v5, s15, v212
	v_cvt_pk_fp8_f32 v6, v4, v5 op_sel:[0,0,1]
	v_med3_f32 v4, v8, s15, v212
	v_med3_f32 v5, v9, s15, v212
	v_cvt_pk_fp8_f32 v7, v4, v5 op_sel:[0,0,1]
	s_mov_b32 s7, 0x24000
	v_add_co_u32_e32 v4, vcc, s7, v2
	v_pk_mul_f32 v[8:9], v[52:53], s[24:25] op_sel_hi:[1,0]
	s_nop 0
	v_addc_co_u32_e32 v5, vcc, 0, v3, vcc
	global_store_dwordx2 v[4:5], v[6:7], off
	v_pk_mul_f32 v[4:5], v[56:57], s[24:25] op_sel_hi:[1,0]
	v_pk_mul_f32 v[6:7], v[54:55], s[24:25] op_sel_hi:[1,0]
	v_pk_mul_f32 v[10:11], v[50:51], s[24:25] op_sel_hi:[1,0]
	v_exp_f32_e32 v6, v6
	v_exp_f32_e32 v7, v7
	v_exp_f32_e32 v4, v4
	v_exp_f32_e32 v5, v5
	v_exp_f32_e32 v10, v10
	v_exp_f32_e32 v8, v8
	v_exp_f32_e32 v9, v9
	v_exp_f32_e32 v11, v11
	v_pk_fma_f32 v[4:5], v[4:5], s[26:27], s[26:27] op_sel_hi:[1,0,0]
	v_pk_fma_f32 v[6:7], v[6:7], s[26:27], s[26:27] op_sel_hi:[1,0,0]
	v_pk_fma_f32 v[8:9], v[8:9], s[26:27], s[26:27] op_sel_hi:[1,0,0]
	v_pk_fma_f32 v[10:11], v[10:11], s[26:27], s[26:27] op_sel_hi:[1,0,0]
	v_rcp_f32_e32 v6, v6
	v_rcp_f32_e32 v7, v7
	v_rcp_f32_e32 v4, v4
	v_rcp_f32_e32 v5, v5
	v_rcp_f32_e32 v10, v10
	v_rcp_f32_e32 v11, v11
	v_rcp_f32_e32 v8, v8
	v_rcp_f32_e32 v9, v9
	v_pk_mul_f32 v[12:13], v[56:57], v[64:65]
	v_pk_mul_f32 v[14:15], v[54:55], v[62:63]
	v_pk_mul_f32 v[4:5], v[12:13], v[4:5]
	v_pk_mul_f32 v[6:7], v[14:15], v[6:7]
	v_pk_mul_f32 v[12:13], v[52:53], v[60:61]
	v_pk_mul_f32 v[14:15], v[50:51], v[58:59]
	v_pk_mul_f32 v[8:9], v[12:13], v[8:9]
	v_pk_mul_f32 v[10:11], v[14:15], v[10:11]
	v_med3_f32 v12, v6, s15, v212
	v_med3_f32 v7, v7, s15, v212
	v_mov_b32_e32 v6, v191
	v_cvt_pk_fp8_f32 v6, v12, v7
	v_med3_f32 v10, v10, s15, v212
	v_med3_f32 v11, v11, s15, v212
	v_mov_b32_e32 v7, v191
	v_cvt_pk_fp8_f32 v7, v10, v11
	v_med3_f32 v4, v4, s15, v212
	v_med3_f32 v5, v5, s15, v212
	v_cvt_pk_fp8_f32 v6, v4, v5 op_sel:[0,0,1]
	v_med3_f32 v4, v8, s15, v212
	v_med3_f32 v5, v9, s15, v212
	v_cvt_pk_fp8_f32 v7, v4, v5 op_sel:[0,0,1]
	s_mov_b32 s7, 0x28000
	v_add_co_u32_e32 v4, vcc, s7, v2
	v_pk_mul_f32 v[8:9], v[36:37], s[24:25] op_sel_hi:[1,0]
	s_nop 0
	v_addc_co_u32_e32 v5, vcc, 0, v3, vcc
	global_store_dwordx2 v[4:5], v[6:7], off
	v_pk_mul_f32 v[4:5], v[40:41], s[24:25] op_sel_hi:[1,0]
	v_pk_mul_f32 v[6:7], v[38:39], s[24:25] op_sel_hi:[1,0]
	v_pk_mul_f32 v[10:11], v[34:35], s[24:25] op_sel_hi:[1,0]
	v_exp_f32_e32 v6, v6
	v_exp_f32_e32 v7, v7
	v_exp_f32_e32 v4, v4
	v_exp_f32_e32 v5, v5
	v_exp_f32_e32 v10, v10
	v_exp_f32_e32 v8, v8
	v_exp_f32_e32 v9, v9
	v_exp_f32_e32 v11, v11
	v_pk_fma_f32 v[4:5], v[4:5], s[26:27], s[26:27] op_sel_hi:[1,0,0]
	v_pk_fma_f32 v[6:7], v[6:7], s[26:27], s[26:27] op_sel_hi:[1,0,0]
	v_pk_fma_f32 v[8:9], v[8:9], s[26:27], s[26:27] op_sel_hi:[1,0,0]
	v_pk_fma_f32 v[10:11], v[10:11], s[26:27], s[26:27] op_sel_hi:[1,0,0]
	v_rcp_f32_e32 v6, v6
	v_rcp_f32_e32 v7, v7
	v_rcp_f32_e32 v4, v4
	v_rcp_f32_e32 v5, v5
	v_rcp_f32_e32 v10, v10
	v_rcp_f32_e32 v11, v11
	v_rcp_f32_e32 v8, v8
	v_rcp_f32_e32 v9, v9
	v_pk_mul_f32 v[12:13], v[40:41], v[48:49]
	v_pk_mul_f32 v[14:15], v[38:39], v[46:47]
	v_pk_mul_f32 v[4:5], v[12:13], v[4:5]
	v_pk_mul_f32 v[6:7], v[14:15], v[6:7]
	v_pk_mul_f32 v[12:13], v[36:37], v[44:45]
	v_pk_mul_f32 v[14:15], v[34:35], v[42:43]
	v_pk_mul_f32 v[8:9], v[12:13], v[8:9]
	v_pk_mul_f32 v[10:11], v[14:15], v[10:11]
	v_med3_f32 v12, v6, s15, v212
	v_med3_f32 v7, v7, s15, v212
	v_mov_b32_e32 v6, v191
	v_cvt_pk_fp8_f32 v6, v12, v7
	v_med3_f32 v10, v10, s15, v212
	v_med3_f32 v11, v11, s15, v212
	v_mov_b32_e32 v7, v191
	v_cvt_pk_fp8_f32 v7, v10, v11
	v_med3_f32 v4, v4, s15, v212
	v_med3_f32 v5, v5, s15, v212
	v_cvt_pk_fp8_f32 v6, v4, v5 op_sel:[0,0,1]
	v_med3_f32 v4, v8, s15, v212
	v_med3_f32 v5, v9, s15, v212
	v_cvt_pk_fp8_f32 v7, v4, v5 op_sel:[0,0,1]
	v_add_co_u32_e32 v2, vcc, 0x2c000, v2
	s_mov_b64 s[10:11], -1
	s_nop 0
	v_addc_co_u32_e32 v3, vcc, 0, v3, vcc
	s_and_b64 vcc, exec, s[36:37]
	global_store_dwordx2 v[2:3], v[6:7], off
	s_cbranch_vccnz .LBB0_1414
	s_andn2_b64 vcc, exec, s[4:5]
	s_cbranch_vccnz .LBB0_1413
	s_barrier
	s_branch .LBB0_1413

; #define GAS __attribute__((address_space(1)))
;     ...
;         if constexpr (FP8) { asm volatile("s_nop 15\n\ts_nop 15\n\ts_nop 15\n\ts_nop 15" ::: "memory"); }
;     __device__ __forceinline__ void operator()(const f32x4 (&acc)[2][2][4][2], const Unit& u, int wr, int wc, int fr, int fq) const {
;         const int b = u.pm < 256 ? (u.pm & 15) : 16;
;         const float* g2 = modL + b * 6144 + 5 * 1024;
;         const int row0 = u.pm * BM + wr * 64 + fr, col0 = (u.pn & 3) * BM + wc * 32 + 8 * fq;
;         constexpr float ds = SC_Y / (SC_W * SC_HID);
;         f32x4 gv[2][2];
; #pragma unroll
;         for (int bj = 0; bj < 2; ++bj)
; #pragma unroll
;             for (int n = 0; n < 2; ++n) gv[bj][n] = *(const f32x4*)(g2 + col0 + bj * HALF + 4 * n) * ds;
;         float gts[2][4];
; #pragma unroll
;         for (int ai = 0; ai < 2; ++ai)
; #pragma unroll
;             for (int m = 0; m < 4; ++m) gts[ai][m] = ((const GAS float*)gate)[row0 + ai * HALF + m * 16];
; #pragma unroll
;         for (int ai = 0; ai < 2; ++ai)
; #pragma unroll
;             for (int m = 0; m < 4; ++m) { const int row = row0 + ai * HALF + m * 16; const float gt = gts[ai][m]; unsigned char* rowp = Y8 + (size_t)row * D + col0;
; #pragma unroll
;                 for (int bj = 0; bj < 2; ++bj) { const f32x4 v0 = acc[ai][bj][m][0] * (gv[bj][0] * gt), v1 = acc[ai][bj][m][1] * (gv[bj][1] * gt); u32x2 w;
;                     w.x = pack4_fp8(v0[0], v0[1], v0[2], v0[3]); w.y = pack4_fp8(v1[0], v1[1], v1[2], v1[3]);
;                     *(u32x2*)(rowp + bj * HALF) = w; } }
.LBB0_1502:
	s_and_b32 s2, s53, 15
	s_cmpk_lt_i32 s53, 0x100
	s_mulk_i32 s2, 0x1800
	s_cselect_b32 s2, s2, 0x18000
	s_lshl_b32 s2, s2, 2
	s_add_u32 s2, s46, s2
	s_addc_u32 s3, s47, 0
	s_lshl_b32 s6, s54, 8
	s_and_b32 s6, s6, 0x300
	v_or_b32_e32 v190, s6, v172
	v_lshlrev_b32_e32 v2, 2, v190
	v_mov_b32_e32 v3, v191
	v_lshl_add_u64 v[2:3], s[2:3], 0, v[2:3]
	s_mov_b64 s[2:3], 0x5000
	v_lshl_add_u64 v[22:23], v[2:3], 0, s[2:3]
	global_load_dwordx4 v[2:5], v[22:23], off
	global_load_dwordx4 v[6:9], v[22:23], off offset:16
	global_load_dwordx4 v[194:197], v[22:23], off offset:512
	global_load_dwordx4 v[198:201], v[22:23], off offset:528
	v_lshl_add_u32 v20, s53, 8, v1
	v_readlane_b32 s2, v252, 11
	v_ashrrev_i32_e32 v21, 31, v20
	v_readlane_b32 s3, v252, 12
	v_or_b32_e32 v170, 16, v20
	v_ashrrev_i32_e32 v171, 31, v170
	v_lshl_add_u64 v[18:19], v[20:21], 2, s[2:3]
	global_load_dword v174, v[18:19], off
	v_lshl_add_u64 v[22:23], v[170:171], 2, s[2:3]
	global_load_dword v168, v[22:23], off
	v_or_b32_e32 v166, 32, v20
	v_ashrrev_i32_e32 v167, 31, v166
	v_lshl_add_u64 v[22:23], v[166:167], 2, s[2:3]
	global_load_dword v32, v[22:23], off
	v_or_b32_e32 v30, 48, v20
	v_ashrrev_i32_e32 v31, 31, v30
	v_lshl_add_u64 v[22:23], v[30:31], 2, s[2:3]
	global_load_dword v28, v[22:23], off
	global_load_dword v26, v[18:19], off offset:512
	global_load_dword v24, v[18:19], off offset:576
	s_nop 0
	global_load_dword v22, v[18:19], off offset:640
	s_nop 0
	global_load_dword v18, v[18:19], off offset:704
	s_nop 15
	s_mov_b32 s2, 0x3d800000
	s_waitcnt vmcnt(0)
	v_pk_mul_f32 v[14:15], v[4:5], s[2:3] op_sel_hi:[1,0]
	v_pk_mul_f32 v[16:17], v[2:3], s[2:3] op_sel_hi:[1,0]
	v_pk_mul_f32 v[10:11], v[8:9], s[2:3] op_sel_hi:[1,0]
	v_pk_mul_f32 v[12:13], v[6:7], s[2:3] op_sel_hi:[1,0]
	v_pk_mul_f32 v[6:7], v[196:197], s[2:3] op_sel_hi:[1,0]
	v_pk_mul_f32 v[8:9], v[194:195], s[2:3] op_sel_hi:[1,0]
	v_pk_mul_f32 v[2:3], v[200:201], s[2:3] op_sel_hi:[1,0]
	v_pk_mul_f32 v[4:5], v[198:199], s[2:3] op_sel_hi:[1,0]
	v_lshlrev_b64 v[20:21], 10, v[20:21]
	v_lshl_add_u64 v[20:21], s[90:91], 0, v[20:21]
	v_lshl_add_u64 v[20:21], v[20:21], 0, v[190:191]
	v_lshlrev_b64 v[30:31], 10, v[30:31]
	v_lshl_add_u64 v[30:31], s[90:91], 0, v[30:31]
	v_lshl_add_u64 v[30:31], v[30:31], 0, v[190:191]
	s_mov_b64 s[2:3], 0x20000
	s_waitcnt vmcnt(7)
	v_pk_mul_f32 v[176:177], v[16:17], v[174:175] op_sel_hi:[1,0]
	s_nop 0
	v_pk_mul_f32 v[154:155], v[154:155], v[176:177]
	v_pk_mul_f32 v[178:179], v[14:15], v[174:175] op_sel_hi:[1,0]
	v_med3_f32 v19, v154, s15, v212
	v_med3_f32 v23, v155, s15, v212
	v_mov_b32_e32 v154, v191
	v_cvt_pk_fp8_f32 v154, v19, v23
	v_pk_mul_f32 v[156:157], v[156:157], v[178:179]
	v_pk_mul_f32 v[178:179], v[12:13], v[174:175] op_sel_hi:[1,0]
	v_med3_f32 v19, v156, s15, v212
	v_pk_mul_f32 v[158:159], v[158:159], v[178:179]
	v_med3_f32 v23, v157, s15, v212
	v_cvt_pk_fp8_f32 v154, v19, v23 op_sel:[0,0,1]
	v_med3_f32 v19, v158, s15, v212
	v_med3_f32 v23, v159, s15, v212
	v_mov_b32_e32 v155, v191
	v_cvt_pk_fp8_f32 v155, v19, v23
	v_pk_mul_f32 v[176:177], v[10:11], v[174:175] op_sel_hi:[1,0]
	v_pk_mul_f32 v[156:157], v[8:9], v[174:175] op_sel_hi:[1,0]
	v_pk_mul_f32 v[160:161], v[160:161], v[176:177]
	v_pk_mul_f32 v[146:147], v[146:147], v[156:157]
	v_med3_f32 v19, v160, s15, v212
	v_med3_f32 v23, v161, s15, v212
	v_cvt_pk_fp8_f32 v155, v19, v23 op_sel:[0,0,1]
	v_med3_f32 v19, v146, s15, v212
	v_med3_f32 v23, v147, s15, v212
	v_mov_b32_e32 v146, v191
	v_cvt_pk_fp8_f32 v146, v19, v23
	global_store_dwordx2 v[20:21], v[154:155], off
	v_pk_mul_f32 v[154:155], v[6:7], v[174:175] op_sel_hi:[1,0]
	v_pk_mul_f32 v[156:157], v[4:5], v[174:175] op_sel_hi:[1,0]
	v_pk_mul_f32 v[148:149], v[148:149], v[154:155]
	v_pk_mul_f32 v[150:151], v[150:151], v[156:157]
	v_med3_f32 v19, v148, s15, v212
	v_med3_f32 v23, v149, s15, v212
	v_cvt_pk_fp8_f32 v146, v19, v23 op_sel:[0,0,1]
	v_med3_f32 v19, v150, s15, v212
	v_med3_f32 v23, v151, s15, v212
	v_mov_b32_e32 v147, v191
	v_cvt_pk_fp8_f32 v147, v19, v23
	v_pk_mul_f32 v[154:155], v[2:3], v[174:175] op_sel_hi:[1,0]
	s_waitcnt vmcnt(7)
	v_pk_mul_f32 v[148:149], v[16:17], v[168:169] op_sel_hi:[1,0]
	v_pk_mul_f32 v[152:153], v[152:153], v[154:155]
	v_pk_mul_f32 v[138:139], v[138:139], v[148:149]
	v_med3_f32 v19, v152, s15, v212
	v_med3_f32 v23, v153, s15, v212
	v_cvt_pk_fp8_f32 v147, v19, v23 op_sel:[0,0,1]
	v_med3_f32 v19, v138, s15, v212
	v_med3_f32 v23, v139, s15, v212
	v_mov_b32_e32 v138, v191
	v_cvt_pk_fp8_f32 v138, v19, v23
	v_pk_mul_f32 v[150:151], v[14:15], v[168:169] op_sel_hi:[1,0]
	v_mov_b32_e32 v139, v191
	v_pk_mul_f32 v[140:141], v[140:141], v[150:151]
	v_pk_mul_f32 v[150:151], v[12:13], v[168:169] op_sel_hi:[1,0]
	v_med3_f32 v19, v140, s15, v212
	v_pk_mul_f32 v[130:131], v[130:131], v[150:151]
	v_med3_f32 v23, v141, s15, v212
	v_cvt_pk_fp8_f32 v138, v19, v23 op_sel:[0,0,1]
	v_med3_f32 v19, v130, s15, v212
	v_med3_f32 v23, v131, s15, v212
	v_pk_mul_f32 v[148:149], v[10:11], v[168:169] op_sel_hi:[1,0]
	v_cvt_pk_fp8_f32 v139, v19, v23
	v_pk_mul_f32 v[132:133], v[132:133], v[148:149]
	v_pk_mul_f32 v[130:131], v[6:7], v[168:169] op_sel_hi:[1,0]
	v_med3_f32 v19, v132, s15, v212
	v_med3_f32 v23, v133, s15, v212
	v_pk_mul_f32 v[132:133], v[8:9], v[168:169] op_sel_hi:[1,0]
	v_cvt_pk_fp8_f32 v139, v19, v23 op_sel:[0,0,1]
	v_pk_mul_f32 v[132:133], v[142:143], v[132:133]
	v_pk_mul_f32 v[130:131], v[144:145], v[130:131]
	v_med3_f32 v19, v132, s15, v212
	v_med3_f32 v23, v133, s15, v212
	v_mov_b32_e32 v132, v191
	v_cvt_pk_fp8_f32 v132, v19, v23
	v_pk_mul_f32 v[140:141], v[4:5], v[168:169] op_sel_hi:[1,0]
	global_store_dwordx2 v[20:21], v[146:147], off offset:128
	v_lshlrev_b64 v[146:147], 10, v[170:171]
	v_pk_mul_f32 v[134:135], v[134:135], v[140:141]
	v_med3_f32 v19, v130, s15, v212
	v_med3_f32 v23, v131, s15, v212
	v_lshl_add_u64 v[146:147], s[90:91], 0, v[146:147]
	v_cvt_pk_fp8_f32 v132, v19, v23 op_sel:[0,0,1]
	v_med3_f32 v19, v134, s15, v212
	v_med3_f32 v23, v135, s15, v212
	v_mov_b32_e32 v133, v191
	v_lshl_add_u64 v[146:147], v[146:147], 0, v[190:191]
	v_cvt_pk_fp8_f32 v133, v19, v23
	global_store_dwordx2 v[146:147], v[138:139], off
	v_pk_mul_f32 v[138:139], v[2:3], v[168:169] op_sel_hi:[1,0]
	s_waitcnt vmcnt(8)
;     __device__ __forceinline__ void operator()(const f32x4 (&acc)[2][2][4][2], const Unit& u, int wr, int wc, int fr, int fq) const {
;     ...
;         for (int ai = 0; ai < 2; ++ai)
; #pragma unroll
;             for (int m = 0; m < 4; ++m) { const int row = row0 + ai * HALF + m * 16; const float gt = gts[ai][m]; unsigned char* rowp = Y8 + (size_t)row * D + col0;
; #pragma unroll
;                 for (int bj = 0; bj < 2; ++bj) { const f32x4 v0 = acc[ai][bj][m][0] * (gv[bj][0] * gt), v1 = acc[ai][bj][m][1] * (gv[bj][1] * gt); u32x2 w;
;                     w.x = pack4_fp8(v0[0], v0[1], v0[2], v0[3]); w.y = pack4_fp8(v1[0], v1[1], v1[2], v1[3]);
;                     *(u32x2*)(rowp + bj * HALF) = w; } }
	v_pk_mul_f32 v[134:135], v[14:15], v[32:33] op_sel_hi:[1,0]
	v_pk_mul_f32 v[136:137], v[136:137], v[138:139]
	v_pk_mul_f32 v[128:129], v[128:129], v[134:135]
	v_med3_f32 v19, v136, s15, v212
	v_med3_f32 v23, v137, s15, v212
	v_cvt_pk_fp8_f32 v133, v19, v23 op_sel:[0,0,1]
	v_pk_mul_f32 v[134:135], v[12:13], v[32:33] op_sel_hi:[1,0]
	v_lshlrev_b64 v[130:131], 10, v[166:167]
	v_pk_mul_f32 v[122:123], v[122:123], v[134:135]
	global_store_dwordx2 v[146:147], v[132:133], off offset:128
	v_pk_mul_f32 v[132:133], v[16:17], v[32:33] op_sel_hi:[1,0]
	v_lshl_add_u64 v[130:131], s[90:91], 0, v[130:131]
	v_pk_mul_f32 v[126:127], v[126:127], v[132:133]
	v_pk_mul_f32 v[132:133], v[10:11], v[32:33] op_sel_hi:[1,0]
	v_med3_f32 v19, v126, s15, v212
	v_med3_f32 v23, v127, s15, v212
	v_mov_b32_e32 v126, v191
	v_cvt_pk_fp8_f32 v126, v19, v23
	v_med3_f32 v19, v128, s15, v212
	v_med3_f32 v23, v129, s15, v212
	v_mov_b32_e32 v127, v191
	v_cvt_pk_fp8_f32 v126, v19, v23 op_sel:[0,0,1]
	v_med3_f32 v19, v122, s15, v212
	v_med3_f32 v23, v123, s15, v212
	v_cvt_pk_fp8_f32 v127, v19, v23
	v_pk_mul_f32 v[124:125], v[124:125], v[132:133]
	v_pk_mul_f32 v[122:123], v[6:7], v[32:33] op_sel_hi:[1,0]
	v_med3_f32 v19, v124, s15, v212
	v_med3_f32 v23, v125, s15, v212
	v_pk_mul_f32 v[124:125], v[8:9], v[32:33] op_sel_hi:[1,0]
	v_pk_mul_f32 v[120:121], v[120:121], v[122:123]
	v_pk_mul_f32 v[118:119], v[118:119], v[124:125]
	v_pk_mul_f32 v[122:123], v[2:3], v[32:33] op_sel_hi:[1,0]
	v_pk_mul_f32 v[32:33], v[4:5], v[32:33] op_sel_hi:[1,0]
	v_cvt_pk_fp8_f32 v127, v19, v23 op_sel:[0,0,1]
	v_pk_mul_f32 v[32:33], v[114:115], v[32:33]
	v_med3_f32 v19, v118, s15, v212
	v_med3_f32 v23, v119, s15, v212
	v_mov_b32_e32 v114, v191
	v_cvt_pk_fp8_f32 v114, v19, v23
	v_med3_f32 v19, v120, s15, v212
	v_med3_f32 v23, v121, s15, v212
	v_mov_b32_e32 v115, v191
	v_cvt_pk_fp8_f32 v114, v19, v23 op_sel:[0,0,1]
	v_med3_f32 v19, v32, s15, v212
	v_med3_f32 v23, v33, s15, v212
	v_cvt_pk_fp8_f32 v115, v19, v23
	v_pk_mul_f32 v[116:117], v[116:117], v[122:123]
	s_waitcnt vmcnt(8)
	v_pk_mul_f32 v[32:33], v[16:17], v[28:29] op_sel_hi:[1,0]
	v_med3_f32 v19, v116, s15, v212
	v_med3_f32 v23, v117, s15, v212
	v_cvt_pk_fp8_f32 v115, v19, v23 op_sel:[0,0,1]
	v_pk_mul_f32 v[32:33], v[110:111], v[32:33]
	v_lshl_add_u64 v[130:131], v[130:131], 0, v[190:191]
	v_med3_f32 v19, v32, s15, v212
	v_med3_f32 v23, v33, s15, v212
	v_mov_b32_e32 v32, v191
	v_cvt_pk_fp8_f32 v32, v19, v23
	global_store_dwordx2 v[130:131], v[114:115], off offset:128
	v_pk_mul_f32 v[114:115], v[14:15], v[28:29] op_sel_hi:[1,0]
	v_mov_b32_e32 v33, v191
	v_pk_mul_f32 v[112:113], v[112:113], v[114:115]
	v_pk_mul_f32 v[114:115], v[12:13], v[28:29] op_sel_hi:[1,0]
	v_med3_f32 v19, v112, s15, v212
	v_pk_mul_f32 v[106:107], v[106:107], v[114:115]
	v_med3_f32 v23, v113, s15, v212
	v_cvt_pk_fp8_f32 v32, v19, v23 op_sel:[0,0,1]
	v_med3_f32 v19, v106, s15, v212
	v_med3_f32 v23, v107, s15, v212
	v_cvt_pk_fp8_f32 v33, v19, v23
	v_pk_mul_f32 v[110:111], v[10:11], v[28:29] op_sel_hi:[1,0]
	v_pk_mul_f32 v[106:107], v[8:9], v[28:29] op_sel_hi:[1,0]
	v_pk_mul_f32 v[108:109], v[108:109], v[110:111]
	v_pk_mul_f32 v[94:95], v[94:95], v[106:107]
	v_med3_f32 v19, v108, s15, v212
	v_med3_f32 v23, v109, s15, v212
	v_cvt_pk_fp8_f32 v33, v19, v23 op_sel:[0,0,1]
	v_med3_f32 v19, v94, s15, v212
	v_med3_f32 v23, v95, s15, v212
	global_store_dwordx2 v[130:131], v[126:127], off
	global_store_dwordx2 v[30:31], v[32:33], off
	v_pk_mul_f32 v[32:33], v[6:7], v[28:29] op_sel_hi:[1,0]
	s_nop 0
	v_pk_mul_f32 v[32:33], v[96:97], v[32:33]
	v_pk_mul_f32 v[96:97], v[2:3], v[28:29] op_sel_hi:[1,0]
	v_pk_mul_f32 v[28:29], v[4:5], v[28:29] op_sel_hi:[1,0]
	v_pk_mul_f32 v[92:93], v[92:93], v[96:97]
	v_pk_mul_f32 v[28:29], v[90:91], v[28:29]
	v_mov_b32_e32 v90, v191
	v_cvt_pk_fp8_f32 v90, v19, v23
	v_med3_f32 v19, v32, s15, v212
	v_med3_f32 v23, v33, s15, v212
	v_mov_b32_e32 v91, v191
	v_cvt_pk_fp8_f32 v90, v19, v23 op_sel:[0,0,1]
	v_med3_f32 v19, v28, s15, v212
	v_med3_f32 v23, v29, s15, v212
	v_cvt_pk_fp8_f32 v91, v19, v23
	v_med3_f32 v19, v92, s15, v212
	v_med3_f32 v23, v93, s15, v212
	s_waitcnt vmcnt(10)
	v_pk_mul_f32 v[32:33], v[14:15], v[26:27] op_sel_hi:[1,0]
	v_cvt_pk_fp8_f32 v91, v19, v23 op_sel:[0,0,1]
	v_pk_mul_f32 v[32:33], v[104:105], v[32:33]
	v_pk_mul_f32 v[92:93], v[12:13], v[26:27] op_sel_hi:[1,0]
	v_lshl_add_u64 v[28:29], v[20:21], 0, s[2:3]
	global_store_dwordx2 v[30:31], v[90:91], off offset:128
	v_pk_mul_f32 v[30:31], v[16:17], v[26:27] op_sel_hi:[1,0]
	v_pk_mul_f32 v[92:93], v[98:99], v[92:93]
	v_pk_mul_f32 v[30:31], v[102:103], v[30:31]
	v_pk_mul_f32 v[90:91], v[10:11], v[26:27] op_sel_hi:[1,0]
	v_med3_f32 v19, v30, s15, v212
	v_med3_f32 v23, v31, s15, v212
	v_mov_b32_e32 v30, v191
	v_cvt_pk_fp8_f32 v30, v19, v23
	v_med3_f32 v19, v32, s15, v212
	v_med3_f32 v23, v33, s15, v212
	v_mov_b32_e32 v31, v191
	v_cvt_pk_fp8_f32 v30, v19, v23 op_sel:[0,0,1]
	v_med3_f32 v19, v92, s15, v212
	v_med3_f32 v23, v93, s15, v212
	v_cvt_pk_fp8_f32 v31, v19, v23
	v_pk_mul_f32 v[90:91], v[100:101], v[90:91]
	s_mov_b32 s2, 0x20000
	v_med3_f32 v19, v90, s15, v212
	v_med3_f32 v23, v91, s15, v212
	v_cvt_pk_fp8_f32 v31, v19, v23 op_sel:[0,0,1]
	v_add_co_u32_e32 v32, vcc, s2, v20
	s_mov_b64 s[2:3], 0x24000
	s_nop 0
	v_addc_co_u32_e32 v33, vcc, 0, v21, vcc
	global_store_dwordx2 v[32:33], v[30:31], off
	v_pk_mul_f32 v[32:33], v[8:9], v[26:27] op_sel_hi:[1,0]
	v_pk_mul_f32 v[30:31], v[6:7], v[26:27] op_sel_hi:[1,0]
	v_pk_mul_f32 v[32:33], v[86:87], v[32:33]
	v_pk_mul_f32 v[30:31], v[88:89], v[30:31]
	v_med3_f32 v19, v32, s15, v212
	v_med3_f32 v23, v33, s15, v212
	v_mov_b32_e32 v32, v191
	v_cvt_pk_fp8_f32 v32, v19, v23
	v_pk_mul_f32 v[86:87], v[2:3], v[26:27] op_sel_hi:[1,0]
	v_pk_mul_f32 v[26:27], v[4:5], v[26:27] op_sel_hi:[1,0]
	v_med3_f32 v19, v30, s15, v212
	v_pk_mul_f32 v[26:27], v[82:83], v[26:27]
	v_med3_f32 v23, v31, s15, v212
	v_cvt_pk_fp8_f32 v32, v19, v23 op_sel:[0,0,1]
	v_med3_f32 v19, v26, s15, v212
	v_med3_f32 v23, v27, s15, v212
	v_mov_b32_e32 v33, v191
	v_cvt_pk_fp8_f32 v33, v19, v23
	v_pk_mul_f32 v[84:85], v[84:85], v[86:87]
	s_waitcnt vmcnt(11)
; #define PG8_BAR __builtin_amdgcn_s_barrier()
;     ...
;         E(acc, cur, wr, wc, fr, fq);
;         if (!has_next) break;
;         cur = nxt; cA = nA; cB = nB; ++ui;
; #pragma unroll
;         for (int _h = 0; _h < 2; ++_h)
; #pragma unroll
;             for (int _i = 0; _i < 2; ++_i) cvo[_h][_i] = nvo[_h][_i];
;         if constexpr (ALIGN_EPI) { if (wr == 1) PG8_BAR; }
;     __device__ __forceinline__ void operator()(const f32x4 (&acc)[2][2][4][2], const Unit& u, int wr, int wc, int fr, int fq) const {
;     ...
;         for (int ai = 0; ai < 2; ++ai)
; #pragma unroll
;             for (int m = 0; m < 4; ++m) { const int row = row0 + ai * HALF + m * 16; const float gt = gts[ai][m]; unsigned char* rowp = Y8 + (size_t)row * D + col0;
; #pragma unroll
;                 for (int bj = 0; bj < 2; ++bj) { const f32x4 v0 = acc[ai][bj][m][0] * (gv[bj][0] * gt), v1 = acc[ai][bj][m][1] * (gv[bj][1] * gt); u32x2 w;
;                     w.x = pack4_fp8(v0[0], v0[1], v0[2], v0[3]); w.y = pack4_fp8(v1[0], v1[1], v1[2], v1[3]);
;                     *(u32x2*)(rowp + bj * HALF) = w; } }
	v_pk_mul_f32 v[30:31], v[14:15], v[24:25] op_sel_hi:[1,0]
	v_med3_f32 v19, v84, s15, v212
	v_med3_f32 v23, v85, s15, v212
	v_cvt_pk_fp8_f32 v33, v19, v23 op_sel:[0,0,1]
	v_pk_mul_f32 v[30:31], v[80:81], v[30:31]
	v_lshl_add_u64 v[26:27], v[20:21], 0, s[2:3]
	s_mov_b32 s2, 0x24000
	global_store_dwordx2 v[28:29], v[32:33], off offset:128
	v_pk_mul_f32 v[28:29], v[16:17], v[24:25] op_sel_hi:[1,0]
	v_pk_mul_f32 v[32:33], v[10:11], v[24:25] op_sel_hi:[1,0]
	v_pk_mul_f32 v[28:29], v[78:79], v[28:29]
	v_pk_mul_f32 v[78:79], v[12:13], v[24:25] op_sel_hi:[1,0]
	v_med3_f32 v19, v28, s15, v212
	v_med3_f32 v23, v29, s15, v212
	v_mov_b32_e32 v28, v191
	v_cvt_pk_fp8_f32 v28, v19, v23
	v_pk_mul_f32 v[74:75], v[74:75], v[78:79]
	v_med3_f32 v19, v30, s15, v212
	v_med3_f32 v23, v31, s15, v212
	v_cvt_pk_fp8_f32 v28, v19, v23 op_sel:[0,0,1]
	v_med3_f32 v19, v74, s15, v212
	v_med3_f32 v23, v75, s15, v212
	v_mov_b32_e32 v29, v191
	v_cvt_pk_fp8_f32 v29, v19, v23
	v_pk_mul_f32 v[32:33], v[76:77], v[32:33]
	v_add_co_u32_e32 v30, vcc, s2, v20
	v_med3_f32 v19, v32, s15, v212
	v_med3_f32 v23, v33, s15, v212
	v_cvt_pk_fp8_f32 v29, v19, v23 op_sel:[0,0,1]
	v_addc_co_u32_e32 v31, vcc, 0, v21, vcc
	v_pk_mul_f32 v[32:33], v[2:3], v[24:25] op_sel_hi:[1,0]
	global_store_dwordx2 v[30:31], v[28:29], off
	v_pk_mul_f32 v[30:31], v[8:9], v[24:25] op_sel_hi:[1,0]
	v_pk_mul_f32 v[28:29], v[6:7], v[24:25] op_sel_hi:[1,0]
	v_pk_mul_f32 v[30:31], v[70:71], v[30:31]
	v_pk_mul_f32 v[28:29], v[72:73], v[28:29]
	v_med3_f32 v19, v30, s15, v212
	v_med3_f32 v23, v31, s15, v212
	v_mov_b32_e32 v30, v191
	v_cvt_pk_fp8_f32 v30, v19, v23
	v_pk_mul_f32 v[24:25], v[4:5], v[24:25] op_sel_hi:[1,0]
	v_med3_f32 v19, v28, s15, v212
	v_pk_mul_f32 v[24:25], v[66:67], v[24:25]
	v_med3_f32 v23, v29, s15, v212
	v_cvt_pk_fp8_f32 v30, v19, v23 op_sel:[0,0,1]
	v_med3_f32 v19, v24, s15, v212
	v_med3_f32 v23, v25, s15, v212
	v_mov_b32_e32 v31, v191
	v_cvt_pk_fp8_f32 v31, v19, v23
	v_pk_mul_f32 v[32:33], v[68:69], v[32:33]
	s_mov_b64 s[2:3], 0x28000
	v_med3_f32 v19, v32, s15, v212
	v_med3_f32 v23, v33, s15, v212
	v_cvt_pk_fp8_f32 v31, v19, v23 op_sel:[0,0,1]
	s_waitcnt vmcnt(12)
	v_pk_mul_f32 v[28:29], v[14:15], v[22:23] op_sel_hi:[1,0]
	v_pk_mul_f32 v[32:33], v[12:13], v[22:23] op_sel_hi:[1,0]
	v_pk_mul_f32 v[28:29], v[64:65], v[28:29]
	global_store_dwordx2 v[26:27], v[30:31], off offset:128
	v_pk_mul_f32 v[26:27], v[16:17], v[22:23] op_sel_hi:[1,0]
	v_pk_mul_f32 v[30:31], v[10:11], v[22:23] op_sel_hi:[1,0]
	v_pk_mul_f32 v[26:27], v[62:63], v[26:27]
	v_pk_mul_f32 v[32:33], v[58:59], v[32:33]
	v_med3_f32 v19, v26, s15, v212
	v_med3_f32 v23, v27, s15, v212
	v_mov_b32_e32 v26, v191
	v_cvt_pk_fp8_f32 v26, v19, v23
	v_med3_f32 v19, v28, s15, v212
	v_med3_f32 v23, v29, s15, v212
	v_mov_b32_e32 v27, v191
	v_cvt_pk_fp8_f32 v26, v19, v23 op_sel:[0,0,1]
	v_med3_f32 v19, v32, s15, v212
	v_med3_f32 v23, v33, s15, v212
	v_cvt_pk_fp8_f32 v27, v19, v23
	v_pk_mul_f32 v[30:31], v[60:61], v[30:31]
	v_lshl_add_u64 v[24:25], v[20:21], 0, s[2:3]
	v_med3_f32 v19, v30, s15, v212
	v_med3_f32 v23, v31, s15, v212
	v_cvt_pk_fp8_f32 v27, v19, v23 op_sel:[0,0,1]
	s_mov_b32 s2, 0x28000
	v_add_co_u32_e32 v28, vcc, s2, v20
	v_pk_mul_f32 v[30:31], v[2:3], v[22:23] op_sel_hi:[1,0]
	s_nop 0
	v_addc_co_u32_e32 v29, vcc, 0, v21, vcc
	global_store_dwordx2 v[28:29], v[26:27], off
	v_pk_mul_f32 v[28:29], v[8:9], v[22:23] op_sel_hi:[1,0]
	v_pk_mul_f32 v[26:27], v[6:7], v[22:23] op_sel_hi:[1,0]
	v_pk_mul_f32 v[28:29], v[54:55], v[28:29]
	v_pk_mul_f32 v[26:27], v[56:57], v[26:27]
	v_med3_f32 v19, v28, s15, v212
	v_med3_f32 v29, v29, s15, v212
	v_mov_b32_e32 v28, v191
	v_cvt_pk_fp8_f32 v28, v19, v29
	v_pk_mul_f32 v[22:23], v[4:5], v[22:23] op_sel_hi:[1,0]
	v_med3_f32 v19, v26, s15, v212
	v_pk_mul_f32 v[22:23], v[50:51], v[22:23]
	v_med3_f32 v26, v27, s15, v212
	v_cvt_pk_fp8_f32 v28, v19, v26 op_sel:[0,0,1]
	v_med3_f32 v19, v22, s15, v212
	v_med3_f32 v22, v23, s15, v212
	v_mov_b32_e32 v29, v191
	v_pk_mul_f32 v[30:31], v[52:53], v[30:31]
	v_cvt_pk_fp8_f32 v29, v19, v22
	v_med3_f32 v19, v30, s15, v212
	s_waitcnt vmcnt(13)
	v_pk_mul_f32 v[16:17], v[16:17], v[18:19] op_sel_hi:[1,0]
	v_med3_f32 v22, v31, s15, v212
	v_pk_mul_f32 v[16:17], v[46:47], v[16:17]
	v_pk_mul_f32 v[12:13], v[12:13], v[18:19] op_sel_hi:[1,0]
	v_cvt_pk_fp8_f32 v29, v19, v22 op_sel:[0,0,1]
	v_pk_mul_f32 v[14:15], v[14:15], v[18:19] op_sel_hi:[1,0]
	v_pk_mul_f32 v[10:11], v[10:11], v[18:19] op_sel_hi:[1,0]
	v_pk_mul_f32 v[12:13], v[42:43], v[12:13]
	v_med3_f32 v19, v16, s15, v212
	v_med3_f32 v17, v17, s15, v212
	v_mov_b32_e32 v16, v191
	v_cvt_pk_fp8_f32 v16, v19, v17
	v_med3_f32 v12, v12, s15, v212
	v_med3_f32 v13, v13, s15, v212
	v_mov_b32_e32 v17, v191
	v_cvt_pk_fp8_f32 v17, v12, v13
	v_pk_mul_f32 v[14:15], v[48:49], v[14:15]
	v_pk_mul_f32 v[10:11], v[44:45], v[10:11]
	v_med3_f32 v14, v14, s15, v212
	v_med3_f32 v15, v15, s15, v212
	v_med3_f32 v10, v10, s15, v212
	v_med3_f32 v11, v11, s15, v212
	s_mov_b64 s[2:3], 0x2c000
	v_cvt_pk_fp8_f32 v16, v14, v15 op_sel:[0,0,1]
	v_cvt_pk_fp8_f32 v17, v10, v11 op_sel:[0,0,1]
	v_lshl_add_u64 v[22:23], v[20:21], 0, s[2:3]
	s_mov_b32 s2, 0x2c000
	v_add_co_u32_e32 v10, vcc, s2, v20
	v_pk_mul_f32 v[8:9], v[8:9], v[18:19] op_sel_hi:[1,0]
	s_nop 0
	v_addc_co_u32_e32 v11, vcc, 0, v21, vcc
	v_pk_mul_f32 v[8:9], v[38:39], v[8:9]
	v_pk_mul_f32 v[4:5], v[4:5], v[18:19] op_sel_hi:[1,0]
	global_store_dwordx2 v[10:11], v[16:17], off
	v_pk_mul_f32 v[4:5], v[34:35], v[4:5]
	v_med3_f32 v10, v8, s15, v212
	v_med3_f32 v9, v9, s15, v212
	v_mov_b32_e32 v8, v191
	v_cvt_pk_fp8_f32 v8, v10, v9
	v_med3_f32 v4, v4, s15, v212
	v_med3_f32 v5, v5, s15, v212
	v_mov_b32_e32 v9, v191
	v_cvt_pk_fp8_f32 v9, v4, v5
	v_pk_mul_f32 v[6:7], v[6:7], v[18:19] op_sel_hi:[1,0]
	v_pk_mul_f32 v[2:3], v[2:3], v[18:19] op_sel_hi:[1,0]
	v_pk_mul_f32 v[6:7], v[40:41], v[6:7]
	v_pk_mul_f32 v[2:3], v[36:37], v[2:3]
	v_med3_f32 v6, v6, s15, v212
	v_med3_f32 v7, v7, s15, v212
	v_med3_f32 v2, v2, s15, v212
	v_med3_f32 v3, v3, s15, v212
	v_cvt_pk_fp8_f32 v8, v6, v7 op_sel:[0,0,1]
	v_cvt_pk_fp8_f32 v9, v2, v3 op_sel:[0,0,1]
	s_mov_b64 s[2:3], -1
	s_andn2_b64 vcc, exec, s[22:23]
	global_store_dwordx2 v[24:25], v[28:29], off offset:128
	global_store_dwordx2 v[22:23], v[8:9], off offset:128
	s_cbranch_vccnz .LBB0_1491
	s_andn2_b64 vcc, exec, s[0:1]
	s_cbranch_vccnz .LBB0_1490
	s_barrier
	s_branch .LBB0_1490
